# gate/up epilogue bias slices fetched one unit ahead and parked in LDS (no vmcnt(0) behind the next unit's staged tiles), on top of the pipelined conversion
# speedup vs baseline: 1.0015x; 1.0015x over previous
.LBB0_801:
	v_and_b32_e32 v5, 15, v4
	s_add_i32 s0, 0, 0x21000
	v_or_b32_e32 v6, s53, v5
	v_lshl_add_u32 v253, v4, 4, s0
	v_and_b32_e32 v7, 48, v4
	v_lshlrev_b32_e32 v8, 6, v6
	s_movk_i32 s0, 0x3c0
	v_and_or_b32 v8, v8, s0, v7
	v_lshlrev_b32_e32 v4, 2, v4
	s_add_u32 s0, s18, 0x80
	v_lshl_or_b32 v5, v5, 6, v7
	v_and_b32_e32 v4, 32, v4
	s_addc_u32 s1, s19, 0
	v_bitop3_b32 v158, v5, s56, v4 bitop3:0xde
	s_waitcnt vmcnt(2)
	s_barrier
	s_add_i32 m0, s7, 0x18000
	v_lshl_add_u64 v[4:5], s[0:1], 0, v[140:141]
	global_load_lds_dwordx4 v[4:5], off
	s_add_i32 m0, s7, 0x1a000
	v_lshl_add_u64 v[4:5], s[0:1], 0, v[142:143]
	s_add_u32 s0, s90, 0x12800080
	s_addc_u32 s1, s91, 0
	s_add_i32 s60, s7, 0x8000
	global_load_lds_dwordx4 v[4:5], off
	s_mov_b32 m0, s60
	v_lshl_add_u64 v[4:5], s[0:1], 0, v[0:1]
	s_add_i32 s61, s7, 0xa000
	global_load_lds_dwordx4 v[4:5], off
	v_lshl_add_u64 v[4:5], s[0:1], 0, v[144:145]
	s_add_u32 s0, s18, 0x40080
	s_mov_b32 m0, s61
	s_addc_u32 s1, s19, 0
	global_load_lds_dwordx4 v[4:5], off
	s_add_i32 m0, s7, 0x1c000
	v_lshl_add_u64 v[4:5], s[0:1], 0, v[140:141]
	global_load_lds_dwordx4 v[4:5], off
	v_lshl_add_u64 v[4:5], s[0:1], 0, v[142:143]
	s_add_i32 m0, s7, 0x1e000
	v_lshlrev_b32_e32 v6, 2, v6
	global_load_lds_dwordx4 v[4:5], off
	v_and_b32_e32 v6, 32, v6
	s_waitcnt vmcnt(6)
	v_readlane_b32 s0, v255, 25
	v_bitop3_b32 v6, v8, s55, v6 bitop3:0xde
	s_cmpk_lt_u32 s0, 0x100
	s_cselect_b64 s[22:23], -1, 0
	s_add_i32 s62, 0, 0x10000
	s_add_i32 s63, 0, 0x14000
	v_add_u32_e32 v143, 0, v6
	v_mov_b32_e32 v145, 0x7f7f7f7f
	s_mov_b32 s24, 0x3c800000
	s_mov_b32 s64, 0xc0c00000
	v_mov_b32_e32 v159, 0x41000000
	v_mov_b32_e32 v4, v141
	v_mov_b32_e32 v5, v141
	v_mov_b32_e32 v6, v141
	v_mov_b32_e32 v7, v141
	v_mov_b32_e32 v8, v141
	v_mov_b32_e32 v9, v141
	v_mov_b32_e32 v10, v141
	v_mov_b32_e32 v11, v141
	s_waitcnt vmcnt(0)
	v_mov_b32_e32 v12, v141
	v_mov_b32_e32 v13, v141
	v_mov_b32_e32 v14, v141
	v_mov_b32_e32 v15, v141
	v_mov_b32_e32 v16, v141
	v_mov_b32_e32 v17, v141
	v_mov_b32_e32 v18, v141
	v_mov_b32_e32 v19, v141
	v_mov_b32_e32 v20, v141
	v_mov_b32_e32 v21, v141
	v_mov_b32_e32 v22, v141
	v_mov_b32_e32 v23, v141
	v_mov_b32_e32 v24, v141
	v_mov_b32_e32 v25, v141
	v_mov_b32_e32 v26, v141
	v_mov_b32_e32 v27, v141
	v_mov_b32_e32 v232, v141
	v_mov_b32_e32 v233, v141
	v_mov_b32_e32 v234, v141
	v_mov_b32_e32 v235, v141
	v_mov_b32_e32 v32, v141
	v_mov_b32_e32 v33, v141
	v_mov_b32_e32 v34, v141
	v_mov_b32_e32 v35, v141
	v_mov_b32_e32 v36, v141
	v_mov_b32_e32 v37, v141
	v_mov_b32_e32 v38, v141
	v_mov_b32_e32 v39, v141
	v_mov_b32_e32 v40, v141
	v_mov_b32_e32 v41, v141
	v_mov_b32_e32 v42, v141
	v_mov_b32_e32 v43, v141
	v_mov_b32_e32 v44, v141
	v_mov_b32_e32 v45, v141
	v_mov_b32_e32 v46, v141
	v_mov_b32_e32 v47, v141
	v_mov_b32_e32 v48, v141
	v_mov_b32_e32 v49, v141
	v_mov_b32_e32 v50, v141
	v_mov_b32_e32 v51, v141
	v_mov_b32_e32 v52, v141
	v_mov_b32_e32 v53, v141
	v_mov_b32_e32 v54, v141
	v_mov_b32_e32 v55, v141
	v_mov_b32_e32 v56, v141
	v_mov_b32_e32 v57, v141
	v_mov_b32_e32 v58, v141
	v_mov_b32_e32 v59, v141
	v_mov_b32_e32 v60, v141
	v_mov_b32_e32 v61, v141
	v_mov_b32_e32 v62, v141
	v_mov_b32_e32 v63, v141
	v_mov_b32_e32 v64, v141
	v_mov_b32_e32 v65, v141
	v_mov_b32_e32 v66, v141
	v_mov_b32_e32 v67, v141
	v_mov_b32_e32 v28, v141
	v_mov_b32_e32 v29, v141
	v_mov_b32_e32 v30, v141
	v_mov_b32_e32 v31, v141
	v_mov_b32_e32 v72, v141
	v_mov_b32_e32 v73, v141
	v_mov_b32_e32 v74, v141
	v_mov_b32_e32 v75, v141
	v_mov_b32_e32 v76, v141
	v_mov_b32_e32 v77, v141
	v_mov_b32_e32 v78, v141
	v_mov_b32_e32 v79, v141
	v_mov_b32_e32 v80, v141
	v_mov_b32_e32 v81, v141
	v_mov_b32_e32 v82, v141
	v_mov_b32_e32 v83, v141
	v_mov_b32_e32 v84, v141
	v_mov_b32_e32 v85, v141
	v_mov_b32_e32 v86, v141
	v_mov_b32_e32 v87, v141
	v_mov_b32_e32 v88, v141
	v_mov_b32_e32 v89, v141
	v_mov_b32_e32 v90, v141
	v_mov_b32_e32 v91, v141
	v_mov_b32_e32 v92, v141
	v_mov_b32_e32 v93, v141
	v_mov_b32_e32 v94, v141
	v_mov_b32_e32 v95, v141
	v_mov_b32_e32 v96, v141
	v_mov_b32_e32 v97, v141
	v_mov_b32_e32 v98, v141
	v_mov_b32_e32 v99, v141
	v_mov_b32_e32 v100, v141
	v_mov_b32_e32 v101, v141
	v_mov_b32_e32 v102, v141
	v_mov_b32_e32 v103, v141
	v_mov_b32_e32 v104, v141
	v_mov_b32_e32 v105, v141
	v_mov_b32_e32 v106, v141
	v_mov_b32_e32 v107, v141
	v_mov_b32_e32 v108, v141
	v_mov_b32_e32 v109, v141
	v_mov_b32_e32 v110, v141
	v_mov_b32_e32 v111, v141
	v_mov_b32_e32 v112, v141
	v_mov_b32_e32 v113, v141
	v_mov_b32_e32 v114, v141
	v_mov_b32_e32 v115, v141
	v_mov_b32_e32 v116, v141
	v_mov_b32_e32 v117, v141
	v_mov_b32_e32 v118, v141
	v_mov_b32_e32 v119, v141
	v_mov_b32_e32 v120, v141
	v_mov_b32_e32 v121, v141
	v_mov_b32_e32 v122, v141
	v_mov_b32_e32 v123, v141
	v_mov_b32_e32 v124, v141
	v_mov_b32_e32 v125, v141
	v_mov_b32_e32 v126, v141
	v_mov_b32_e32 v127, v141
	v_mov_b32_e32 v128, v141
	v_mov_b32_e32 v129, v141
	v_mov_b32_e32 v130, v141
	v_mov_b32_e32 v131, v141
	s_barrier
	v_mbcnt_lo_u32_b32 v200, -1, 0
	v_mbcnt_hi_u32_b32 v200, -1, v200
	v_lshrrev_b32_e32 v200, 4, v200
	v_readlane_b32 s98, v255, 35
	v_readlane_b32 s99, v255, 36
	v_readlane_b32 s100, v255, 39
	v_readlane_b32 s101, v255, 40
	s_lshl_b32 vcc_lo, s4, 13
	s_add_u32 s98, s98, vcc_lo
	s_addc_u32 s99, s99, 0
	s_add_u32 s100, s100, vcc_lo
	s_addc_u32 s101, s101, 0
	s_lshl_b32 vcc_lo, s6, 7
	s_or_b32 vcc_lo, vcc_lo, s54
	v_lshl_add_u32 v201, v200, 3, vcc_lo
	v_lshlrev_b32_e32 v201, 2, v201
	global_load_dwordx4 v[184:187], v201, s[98:99]
	global_load_dwordx4 v[188:191], v201, s[98:99] offset:16
	global_load_dwordx4 v[192:195], v201, s[100:101]
	global_load_dwordx4 v[196:199], v201, s[100:101] offset:16
	v_lshl_add_u32 v204, v200, 3, s54
	v_lshlrev_b32_e32 v204, 2, v204
	s_and_b32 vcc_lo, s59, 1
	s_lshl_b32 vcc_lo, vcc_lo, 10
	s_add_u32 vcc_lo, vcc_lo, 0x26800
	v_add_u32_e32 v204, vcc_lo, v204
	s_waitcnt vmcnt(0)
	ds_write_b128 v204, v[184:187]
	ds_write_b128 v204, v[188:191] offset:16
	ds_write_b128 v204, v[192:195] offset:512
	ds_write_b128 v204, v[196:199] offset:528
	s_branch .LBB0_804

.LBB0_837:
	s_lshl_b32 s5, s6, 7
	v_mbcnt_lo_u32_b32 v1, -1, 0
	v_mbcnt_hi_u32_b32 v1, -1, v1
	s_or_b32 s5, s5, s54
	v_ashrrev_i32_e32 v141, 4, v1
	v_lshl_add_u32 v146, v141, 3, s5
	s_ashr_i32 s5, s4, 31
	v_readlane_b32 s72, v255, 31
	s_lshl_b64 s[38:39], s[4:5], 13
	v_readlane_b32 s76, v255, 35
	v_readlane_b32 s77, v255, 36
	s_add_u32 s40, s76, s38
	v_readlane_b32 s80, v255, 39
	s_addc_u32 s41, s77, s39
	v_ashrrev_i32_e32 v147, 31, v146
	v_readlane_b32 s81, v255, 40
	v_lshlrev_b64 v[68:69], 2, v[146:147]
	s_add_u32 s38, s80, s38
	v_lshl_add_u64 v[70:71], s[40:41], 0, v[68:69]
	s_addc_u32 s39, s81, s39
	s_lshl_b32 s98, s6, 7
	v_subrev_u32_e32 v204, s98, v146
	v_lshlrev_b32_e32 v204, 2, v204
	s_and_b32 s99, s59, 1
	s_lshl_b32 s99, s99, 10
	s_add_u32 s99, s99, 0x26800
	v_add_u32_e32 v204, s99, v204
	ds_read_b128 v[136:139], v204
	ds_read_b128 v[132:135], v204 offset:16
	v_lshl_add_u64 v[148:149], s[38:39], 0, v[68:69]
	ds_read_b128 v[68:71], v204 offset:512
	ds_read_b128 v[160:163], v204 offset:528
	s_cmp_lg_u32 s36, 0
	s_cbranch_scc0 .Lnb_skip_p6a
	s_lshl_b32 s98, s28, 7
	s_or_b32 s98, s98, s54
	v_lshl_add_u32 v200, v141, 3, s98
	v_lshlrev_b32_e32 v200, 2, v200
	s_lshl_b32 s98, s26, 13
	s_add_u32 s100, s80, s98
	s_addc_u32 s101, s81, 0
	s_add_u32 s98, s76, s98
	s_addc_u32 s99, s77, 0
	global_load_dwordx4 v[184:187], v200, s[98:99]
	global_load_dwordx4 v[188:191], v200, s[98:99] offset:16
	global_load_dwordx4 v[192:195], v200, s[100:101]
	global_load_dwordx4 v[196:199], v200, s[100:101] offset:16
.Lnb_skip_p6a:
	v_and_b32_e32 v141, 1, v141
	v_and_b32_e32 v1, 15, v1
	v_lshlrev_b32_e32 v150, 4, v141
	s_add_i32 s5, s2, s53
	v_add3_u32 v150, s5, v1, v150
	v_ashrrev_i32_e32 v151, 31, v150
	v_lshlrev_b32_e32 v141, 3, v141
	v_lshlrev_b64 v[150:151], 11, v[150:151]
	v_sub_co_u32_e32 v148, vcc, 0, v141
	v_lshl_add_u64 v[150:151], s[14:15], 0, v[150:151]
	v_lshl_add_u64 v[146:147], v[150:151], 0, v[146:147]
	v_subb_co_u32_e64 v149, s[38:39], 0, 0, vcc
	v_lshl_add_u64 v[146:147], v[146:147], 0, v[148:149]
	v_mov_b32_e32 v164, 0
	v_mov_b32_e32 v165, 0
	s_mov_b32 s5, 0x10000
	v_readlane_b32 s73, v255, 32
	v_readlane_b32 s74, v255, 33
	v_readlane_b32 s75, v255, 34
	v_readlane_b32 s78, v255, 37
	v_readlane_b32 s79, v255, 38
	v_readlane_b32 s82, v255, 41
	v_readlane_b32 s83, v255, 42
	v_readlane_b32 s84, v255, 43
	v_readlane_b32 s85, v255, 44
	v_readlane_b32 s86, v255, 45
	v_readlane_b32 s87, v255, 46
	s_waitcnt lgkmcnt(0)
	v_pk_fma_f32 v[166:167], v[128:129], s[24:25], v[136:137] op_sel_hi:[1,0,1]
	v_pk_fma_f32 v[156:157], v[130:131], s[24:25], v[138:139] op_sel_hi:[1,0,1]
	v_pk_add_f32 v[154:155], v[68:69], 1.0 op_sel_hi:[1,0]
	v_min_f32_e32 v68, 0x40e00000, v166
	v_min_f32_e32 v69, 0x40e00000, v167
	v_pk_fma_f32 v[168:169], v[126:127], s[24:25], v[134:135] op_sel_hi:[1,0,1]
	v_mul_f32_e32 v1, 0xc01d265f, v68
	v_mul_f32_e32 v141, 0xc01d265f, v69
	v_pk_add_f32 v[152:153], v[70:71], 1.0 op_sel_hi:[1,0]
	v_pk_add_f32 v[150:151], v[160:161], 1.0 op_sel_hi:[1,0]
	v_min_f32_e32 v70, 0x40e00000, v156
	v_min_f32_e32 v71, 0x40e00000, v157
	v_min_f32_e32 v160, 0x40e00000, v168
	v_min_f32_e32 v161, 0x40e00000, v169
	v_exp_f32_e32 v174, v1
	v_exp_f32_e32 v175, v141
	v_mul_f32_e32 v176, 0xc01d265f, v70
	v_mul_f32_e32 v177, 0xc01d265f, v71
	v_mul_f32_e32 v180, 0xc01d265f, v160
	v_mul_f32_e32 v181, 0xc01d265f, v161
	v_exp_f32_e32 v176, v176
	v_exp_f32_e32 v177, v177
	v_exp_f32_e32 v180, v180
	v_exp_f32_e32 v181, v181
	v_pk_add_f32 v[174:175], v[174:175], 1.0 op_sel_hi:[1,0]
	v_pk_fma_f32 v[170:171], v[124:125], s[24:25], v[132:133] op_sel_hi:[1,0,1]
	v_rcp_f32_e32 v174, v174
	v_rcp_f32_e32 v175, v175
	v_min_f32_e32 v156, 0x40e00000, v170
	v_min_f32_e32 v157, 0x40e00000, v171
	v_pk_add_f32 v[176:177], v[176:177], 1.0 op_sel_hi:[1,0]
	v_pk_add_f32 v[180:181], v[180:181], 1.0 op_sel_hi:[1,0]
	v_mul_f32_e32 v178, 0xc01d265f, v156
	v_mul_f32_e32 v179, 0xc01d265f, v157
	v_rcp_f32_e32 v176, v176
	v_rcp_f32_e32 v177, v177
	v_rcp_f32_e32 v180, v180
	v_rcp_f32_e32 v181, v181
	v_pk_fma_f32 v[166:167], v[96:97], s[24:25], v[154:155] op_sel_hi:[1,0,1]
	v_exp_f32_e32 v178, v178
	v_exp_f32_e32 v179, v179
	v_pk_add_f32 v[148:149], v[162:163], 1.0 op_sel_hi:[1,0]
	v_med3_f32 v166, v166, s64, v159
	v_med3_f32 v167, v167, s64, v159
	v_pk_mul_f32 v[68:69], v[68:69], v[174:175]
	v_pk_fma_f32 v[162:163], v[98:99], s[24:25], v[152:153] op_sel_hi:[1,0,1]
	v_pk_fma_f32 v[168:169], v[94:95], s[24:25], v[148:149] op_sel_hi:[1,0,1]
	v_pk_mul_f32 v[68:69], v[166:167], v[68:69]
	v_pk_fma_f32 v[172:173], v[122:123], s[24:25], v[138:139] op_sel_hi:[1,0,1]
	v_med3_f32 v162, v162, s64, v159
	v_med3_f32 v163, v163, s64, v159
	v_med3_f32 v168, v168, s64, v159
	v_med3_f32 v169, v169, s64, v159
	v_pk_mul_f32 v[70:71], v[70:71], v[176:177]
	v_pk_mul_f32 v[160:161], v[160:161], v[180:181]
	v_cvt_pk_fp8_f32 v164, v68, v69
	v_pk_add_f32 v[178:179], v[178:179], 1.0 op_sel_hi:[1,0]
	v_pk_mul_f32 v[68:69], v[162:163], v[70:71]
	v_pk_mul_f32 v[70:71], v[168:169], v[160:161]
	v_min_f32_e32 v160, 0x40e00000, v172
	v_rcp_f32_e32 v178, v178
	v_rcp_f32_e32 v179, v179
	v_min_f32_e32 v161, 0x40e00000, v173
	v_mul_f32_e32 v141, 0xc01d265f, v160
	v_exp_f32_e32 v166, v141
	v_mul_f32_e32 v141, 0xc01d265f, v161
	v_cvt_pk_fp8_f32 v164, v68, v69 op_sel:[0,0,1]
	v_pk_fma_f32 v[68:69], v[120:121], s[24:25], v[136:137] op_sel_hi:[1,0,1]
	v_exp_f32_e32 v167, v141
	v_pk_fma_f32 v[170:171], v[92:93], s[24:25], v[150:151] op_sel_hi:[1,0,1]
	v_min_f32_e32 v68, 0x40e00000, v68
	v_med3_f32 v170, v170, s64, v159
	v_med3_f32 v171, v171, s64, v159
	v_pk_mul_f32 v[156:157], v[156:157], v[178:179]
	v_min_f32_e32 v69, 0x40e00000, v69
	v_mul_f32_e32 v1, 0xc01d265f, v68
	v_pk_mul_f32 v[156:157], v[170:171], v[156:157]
	v_exp_f32_e32 v162, v1
	v_mul_f32_e32 v1, 0xc01d265f, v69
	v_cvt_pk_fp8_f32 v165, v156, v157
	v_exp_f32_e32 v163, v1
	v_pk_add_f32 v[166:167], v[166:167], 1.0 op_sel_hi:[1,0]
	v_pk_fma_f32 v[156:157], v[88:89], s[24:25], v[154:155] op_sel_hi:[1,0,1]
	v_rcp_f32_e32 v166, v166
	v_rcp_f32_e32 v167, v167
	v_cvt_pk_fp8_f32 v165, v70, v71 op_sel:[0,0,1]
	v_pk_fma_f32 v[70:71], v[90:91], s[24:25], v[152:153] op_sel_hi:[1,0,1]
	v_pk_add_f32 v[162:163], v[162:163], 1.0 op_sel_hi:[1,0]
	v_med3_f32 v70, v70, s64, v159
	v_rcp_f32_e32 v162, v162
	v_rcp_f32_e32 v163, v163
	v_med3_f32 v71, v71, s64, v159
	v_pk_mul_f32 v[160:161], v[160:161], v[166:167]
	v_med3_f32 v156, v156, s64, v159
	v_pk_mul_f32 v[70:71], v[70:71], v[160:161]
	v_pk_fma_f32 v[160:161], v[116:117], s[24:25], v[132:133] op_sel_hi:[1,0,1]
	v_med3_f32 v157, v157, s64, v159
	v_min_f32_e32 v160, 0x40e00000, v160
	v_min_f32_e32 v161, 0x40e00000, v161
	v_mul_f32_e32 v1, 0xc01d265f, v160
	v_pk_mul_f32 v[68:69], v[68:69], v[162:163]
	v_exp_f32_e32 v168, v1
	v_mul_f32_e32 v1, 0xc01d265f, v161
	v_pk_mul_f32 v[68:69], v[156:157], v[68:69]
	v_pk_fma_f32 v[156:157], v[118:119], s[24:25], v[134:135] op_sel_hi:[1,0,1]
	v_exp_f32_e32 v169, v1
	v_min_f32_e32 v156, 0x40e00000, v156
	v_min_f32_e32 v157, 0x40e00000, v157
	v_mul_f32_e32 v1, 0xc01d265f, v156
	v_exp_f32_e32 v170, v1
	v_mul_f32_e32 v1, 0xc01d265f, v157
	v_exp_f32_e32 v171, v1
	v_pk_add_f32 v[168:169], v[168:169], 1.0 op_sel_hi:[1,0]
	v_pk_fma_f32 v[166:167], v[84:85], s[24:25], v[150:151] op_sel_hi:[1,0,1]
	v_rcp_f32_e32 v168, v168
	v_rcp_f32_e32 v169, v169
	v_pk_add_f32 v[170:171], v[170:171], 1.0 op_sel_hi:[1,0]
	v_med3_f32 v166, v166, s64, v159
	v_med3_f32 v167, v167, s64, v159
	v_rcp_f32_e32 v170, v170
	v_rcp_f32_e32 v171, v171
	v_pk_mul_f32 v[160:161], v[160:161], v[168:169]
	v_pk_fma_f32 v[162:163], v[86:87], s[24:25], v[148:149] op_sel_hi:[1,0,1]
	v_pk_mul_f32 v[160:161], v[166:167], v[160:161]
	v_mov_b32_e32 v166, 0
	v_mov_b32_e32 v167, 0
	v_cvt_pk_fp8_f32 v166, v68, v69
	v_cvt_pk_fp8_f32 v167, v160, v161
	v_med3_f32 v162, v162, s64, v159
	v_med3_f32 v163, v163, s64, v159
	v_pk_mul_f32 v[68:69], v[156:157], v[170:171]
	v_cvt_pk_fp8_f32 v166, v70, v71 op_sel:[0,0,1]
	v_pk_mul_f32 v[68:69], v[162:163], v[68:69]
	v_pk_fma_f32 v[70:71], v[112:113], s[24:25], v[136:137] op_sel_hi:[1,0,1]
	v_cvt_pk_fp8_f32 v167, v68, v69 op_sel:[0,0,1]
	v_min_f32_e32 v70, 0x40e00000, v70
	v_pk_fma_f32 v[68:69], v[114:115], s[24:25], v[138:139] op_sel_hi:[1,0,1]
	v_min_f32_e32 v71, 0x40e00000, v71
	v_mul_f32_e32 v1, 0xc01d265f, v70
	v_min_f32_e32 v68, 0x40e00000, v68
	v_exp_f32_e32 v162, v1
	v_mul_f32_e32 v1, 0xc01d265f, v71
	v_permlane16_swap_b32_e32 v164, v166
	v_permlane16_swap_b32_e32 v165, v167
	v_min_f32_e32 v69, 0x40e00000, v69
	v_mul_f32_e32 v141, 0xc01d265f, v68
	v_exp_f32_e32 v163, v1
	global_store_dwordx4 v[146:147], v[164:167], off
	v_pk_fma_f32 v[160:161], v[80:81], s[24:25], v[154:155] op_sel_hi:[1,0,1]
	v_pk_fma_f32 v[156:157], v[82:83], s[24:25], v[152:153] op_sel_hi:[1,0,1]
	v_exp_f32_e32 v164, v141
	v_mul_f32_e32 v141, 0xc01d265f, v69
	v_exp_f32_e32 v165, v141
	v_pk_add_f32 v[162:163], v[162:163], 1.0 op_sel_hi:[1,0]
	v_med3_f32 v160, v160, s64, v159
	v_rcp_f32_e32 v162, v162
	v_rcp_f32_e32 v163, v163
	v_pk_add_f32 v[164:165], v[164:165], 1.0 op_sel_hi:[1,0]
	v_med3_f32 v161, v161, s64, v159
	v_rcp_f32_e32 v164, v164
	v_rcp_f32_e32 v165, v165
	v_pk_mul_f32 v[70:71], v[70:71], v[162:163]
	v_med3_f32 v156, v156, s64, v159
	v_pk_mul_f32 v[70:71], v[160:161], v[70:71]
	v_pk_fma_f32 v[160:161], v[108:109], s[24:25], v[132:133] op_sel_hi:[1,0,1]
	v_med3_f32 v157, v157, s64, v159
	v_pk_mul_f32 v[68:69], v[68:69], v[164:165]
	v_min_f32_e32 v160, 0x40e00000, v160
	v_pk_mul_f32 v[156:157], v[156:157], v[68:69]
	v_pk_fma_f32 v[68:69], v[110:111], s[24:25], v[134:135] op_sel_hi:[1,0,1]
	v_min_f32_e32 v161, 0x40e00000, v161
	v_mul_f32_e32 v1, 0xc01d265f, v160
	v_min_f32_e32 v166, 0x40e00000, v68
	v_exp_f32_e32 v68, v1
	v_mul_f32_e32 v1, 0xc01d265f, v161
	v_min_f32_e32 v167, 0x40e00000, v69
	v_exp_f32_e32 v69, v1
	v_mul_f32_e32 v1, 0xc01d265f, v166
	v_exp_f32_e32 v168, v1
	v_mul_f32_e32 v1, 0xc01d265f, v167
	v_pk_add_f32 v[68:69], v[68:69], 1.0 op_sel_hi:[1,0]
	v_exp_f32_e32 v169, v1
	v_rcp_f32_e32 v68, v68
	v_rcp_f32_e32 v69, v69
	v_pk_fma_f32 v[164:165], v[76:77], s[24:25], v[150:151] op_sel_hi:[1,0,1]
	v_pk_add_f32 v[168:169], v[168:169], 1.0 op_sel_hi:[1,0]
	v_med3_f32 v164, v164, s64, v159
	v_med3_f32 v165, v165, s64, v159
	v_pk_mul_f32 v[68:69], v[160:161], v[68:69]
	v_rcp_f32_e32 v168, v168
	v_pk_mul_f32 v[160:161], v[164:165], v[68:69]
	v_mov_b32_e32 v68, 0
	v_rcp_f32_e32 v169, v169
	v_cvt_pk_fp8_f32 v68, v70, v71
	v_mov_b32_e32 v69, 0
	v_cvt_pk_fp8_f32 v69, v160, v161
	v_pk_fma_f32 v[162:163], v[78:79], s[24:25], v[148:149] op_sel_hi:[1,0,1]
	v_pk_mul_f32 v[70:71], v[166:167], v[168:169]
	v_med3_f32 v162, v162, s64, v159
	v_med3_f32 v163, v163, s64, v159
	v_cvt_pk_fp8_f32 v68, v156, v157 op_sel:[0,0,1]
	v_pk_fma_f32 v[156:157], v[104:105], s[24:25], v[136:137] op_sel_hi:[1,0,1]
	v_pk_mul_f32 v[70:71], v[162:163], v[70:71]
	v_min_f32_e32 v156, 0x40e00000, v156
	v_cvt_pk_fp8_f32 v69, v70, v71 op_sel:[0,0,1]
	v_pk_fma_f32 v[70:71], v[106:107], s[24:25], v[138:139] op_sel_hi:[1,0,1]
	v_min_f32_e32 v157, 0x40e00000, v157
	v_mul_f32_e32 v1, 0xc01d265f, v156
	v_min_f32_e32 v70, 0x40e00000, v70
	v_exp_f32_e32 v164, v1
	v_mul_f32_e32 v1, 0xc01d265f, v157
	v_min_f32_e32 v71, 0x40e00000, v71
	v_mul_f32_e32 v141, 0xc01d265f, v70
	v_exp_f32_e32 v165, v1
	v_exp_f32_e32 v166, v141
	v_mul_f32_e32 v141, 0xc01d265f, v71
	v_exp_f32_e32 v167, v141
	v_pk_add_f32 v[164:165], v[164:165], 1.0 op_sel_hi:[1,0]
	v_pk_fma_f32 v[162:163], v[72:73], s[24:25], v[154:155] op_sel_hi:[1,0,1]
	v_rcp_f32_e32 v164, v164
	v_rcp_f32_e32 v165, v165
	v_pk_add_f32 v[166:167], v[166:167], 1.0 op_sel_hi:[1,0]
	v_med3_f32 v162, v162, s64, v159
	v_rcp_f32_e32 v166, v166
	v_rcp_f32_e32 v167, v167
	v_med3_f32 v163, v163, s64, v159
	v_pk_mul_f32 v[156:157], v[156:157], v[164:165]
	v_pk_fma_f32 v[160:161], v[74:75], s[24:25], v[152:153] op_sel_hi:[1,0,1]
	v_pk_mul_f32 v[156:157], v[162:163], v[156:157]
	v_pk_fma_f32 v[162:163], v[100:101], s[24:25], v[132:133] op_sel_hi:[1,0,1]
	v_med3_f32 v160, v160, s64, v159
	v_med3_f32 v161, v161, s64, v159
	v_pk_mul_f32 v[70:71], v[70:71], v[166:167]
	v_min_f32_e32 v162, 0x40e00000, v162
	v_pk_mul_f32 v[160:161], v[160:161], v[70:71]
	v_pk_fma_f32 v[70:71], v[102:103], s[24:25], v[134:135] op_sel_hi:[1,0,1]
	v_min_f32_e32 v163, 0x40e00000, v163
	v_mul_f32_e32 v1, 0xc01d265f, v162
	v_min_f32_e32 v168, 0x40e00000, v70
	v_exp_f32_e32 v70, v1
	v_mul_f32_e32 v1, 0xc01d265f, v163
	v_min_f32_e32 v169, 0x40e00000, v71
	v_exp_f32_e32 v71, v1
	v_mul_f32_e32 v1, 0xc01d265f, v168
	v_exp_f32_e32 v170, v1
	v_mul_f32_e32 v1, 0xc01d265f, v169
	v_exp_f32_e32 v171, v1
	v_pk_add_f32 v[70:71], v[70:71], 1.0 op_sel_hi:[1,0]
	v_pk_fma_f32 v[166:167], v[28:29], s[24:25], v[150:151] op_sel_hi:[1,0,1]
	v_rcp_f32_e32 v70, v70
	v_rcp_f32_e32 v71, v71
	v_pk_add_f32 v[170:171], v[170:171], 1.0 op_sel_hi:[1,0]
	v_med3_f32 v166, v166, s64, v159
	v_med3_f32 v167, v167, s64, v159
	v_rcp_f32_e32 v170, v170
	v_rcp_f32_e32 v171, v171
	v_pk_mul_f32 v[70:71], v[162:163], v[70:71]
	v_pk_fma_f32 v[164:165], v[30:31], s[24:25], v[148:149] op_sel_hi:[1,0,1]
	v_pk_mul_f32 v[162:163], v[166:167], v[70:71]
	v_mov_b32_e32 v70, 0
	v_mov_b32_e32 v71, 0
	v_cvt_pk_fp8_f32 v70, v156, v157
	v_cvt_pk_fp8_f32 v71, v162, v163
	v_med3_f32 v164, v164, s64, v159
	v_med3_f32 v165, v165, s64, v159
	v_pk_mul_f32 v[156:157], v[168:169], v[170:171]
	v_cvt_pk_fp8_f32 v70, v160, v161 op_sel:[0,0,1]
	v_pk_mul_f32 v[156:157], v[164:165], v[156:157]
	v_pk_fma_f32 v[160:161], v[32:33], s[24:25], v[154:155] op_sel_hi:[1,0,1]
	v_cvt_pk_fp8_f32 v71, v156, v157 op_sel:[0,0,1]
	v_add_co_u32_e32 v156, vcc, s5, v146
	v_permlane16_swap_b32_e32 v68, v70
	v_permlane16_swap_b32_e32 v69, v71
	v_addc_co_u32_e32 v157, vcc, 0, v147, vcc
	global_store_dwordx4 v[156:157], v[68:71], off
	v_med3_f32 v160, v160, s64, v159
	v_med3_f32 v161, v161, s64, v159
	v_pk_fma_f32 v[70:71], v[64:65], s[24:25], v[136:137] op_sel_hi:[1,0,1]
	v_pk_fma_f32 v[68:69], v[66:67], s[24:25], v[138:139] op_sel_hi:[1,0,1]
	v_min_f32_e32 v70, 0x40e00000, v70
	v_min_f32_e32 v71, 0x40e00000, v71
	v_mul_f32_e32 v1, 0xc01d265f, v70
	v_min_f32_e32 v68, 0x40e00000, v68
	v_exp_f32_e32 v162, v1
	v_mul_f32_e32 v1, 0xc01d265f, v71
	v_min_f32_e32 v69, 0x40e00000, v69
	v_mul_f32_e32 v141, 0xc01d265f, v68
	v_exp_f32_e32 v163, v1
	v_exp_f32_e32 v164, v141
	v_mul_f32_e32 v141, 0xc01d265f, v69
	v_exp_f32_e32 v165, v141
	v_pk_add_f32 v[162:163], v[162:163], 1.0 op_sel_hi:[1,0]
	v_pk_fma_f32 v[156:157], v[34:35], s[24:25], v[152:153] op_sel_hi:[1,0,1]
	v_rcp_f32_e32 v162, v162
	v_rcp_f32_e32 v163, v163
	v_pk_add_f32 v[164:165], v[164:165], 1.0 op_sel_hi:[1,0]
	v_med3_f32 v156, v156, s64, v159
	v_rcp_f32_e32 v164, v164
	v_rcp_f32_e32 v165, v165
	v_pk_mul_f32 v[70:71], v[70:71], v[162:163]
	v_med3_f32 v157, v157, s64, v159
	v_pk_mul_f32 v[70:71], v[160:161], v[70:71]
	v_pk_fma_f32 v[160:161], v[60:61], s[24:25], v[132:133] op_sel_hi:[1,0,1]
	v_pk_mul_f32 v[68:69], v[68:69], v[164:165]
	v_min_f32_e32 v160, 0x40e00000, v160
	v_pk_mul_f32 v[156:157], v[156:157], v[68:69]
	v_pk_fma_f32 v[68:69], v[62:63], s[24:25], v[134:135] op_sel_hi:[1,0,1]
	v_min_f32_e32 v161, 0x40e00000, v161
	v_mul_f32_e32 v1, 0xc01d265f, v160
	v_min_f32_e32 v166, 0x40e00000, v68
	v_exp_f32_e32 v68, v1
	v_mul_f32_e32 v1, 0xc01d265f, v161
	v_min_f32_e32 v167, 0x40e00000, v69
	v_exp_f32_e32 v69, v1
	v_mul_f32_e32 v1, 0xc01d265f, v166
	v_exp_f32_e32 v168, v1
	v_mul_f32_e32 v1, 0xc01d265f, v167
	v_pk_add_f32 v[68:69], v[68:69], 1.0 op_sel_hi:[1,0]
	v_exp_f32_e32 v169, v1
	v_rcp_f32_e32 v68, v68
	v_rcp_f32_e32 v69, v69
	v_pk_fma_f32 v[164:165], v[232:233], s[24:25], v[150:151] op_sel_hi:[1,0,1]
	v_pk_add_f32 v[168:169], v[168:169], 1.0 op_sel_hi:[1,0]
	v_med3_f32 v164, v164, s64, v159
	v_med3_f32 v165, v165, s64, v159
	v_pk_mul_f32 v[68:69], v[160:161], v[68:69]
	v_rcp_f32_e32 v168, v168
	v_pk_mul_f32 v[160:161], v[164:165], v[68:69]
	v_mov_b32_e32 v68, 0
	v_rcp_f32_e32 v169, v169
	v_cvt_pk_fp8_f32 v68, v70, v71
	v_mov_b32_e32 v69, 0
	v_cvt_pk_fp8_f32 v69, v160, v161
	v_pk_fma_f32 v[162:163], v[234:235], s[24:25], v[148:149] op_sel_hi:[1,0,1]
	v_pk_mul_f32 v[70:71], v[166:167], v[168:169]
	v_med3_f32 v162, v162, s64, v159
	v_med3_f32 v163, v163, s64, v159
	v_cvt_pk_fp8_f32 v68, v156, v157 op_sel:[0,0,1]
	v_pk_fma_f32 v[156:157], v[56:57], s[24:25], v[136:137] op_sel_hi:[1,0,1]
	v_pk_mul_f32 v[70:71], v[162:163], v[70:71]
	v_min_f32_e32 v156, 0x40e00000, v156
	v_cvt_pk_fp8_f32 v69, v70, v71 op_sel:[0,0,1]
	v_pk_fma_f32 v[70:71], v[58:59], s[24:25], v[138:139] op_sel_hi:[1,0,1]
	v_min_f32_e32 v157, 0x40e00000, v157
	v_mul_f32_e32 v1, 0xc01d265f, v156
	v_min_f32_e32 v70, 0x40e00000, v70
	v_exp_f32_e32 v164, v1
	v_mul_f32_e32 v1, 0xc01d265f, v157
	v_min_f32_e32 v71, 0x40e00000, v71
	v_mul_f32_e32 v141, 0xc01d265f, v70
	v_exp_f32_e32 v165, v1
	v_exp_f32_e32 v166, v141
	v_mul_f32_e32 v141, 0xc01d265f, v71
	v_exp_f32_e32 v167, v141
	v_pk_add_f32 v[164:165], v[164:165], 1.0 op_sel_hi:[1,0]
	v_pk_fma_f32 v[162:163], v[24:25], s[24:25], v[154:155] op_sel_hi:[1,0,1]
	v_rcp_f32_e32 v164, v164
	v_rcp_f32_e32 v165, v165
	v_pk_add_f32 v[166:167], v[166:167], 1.0 op_sel_hi:[1,0]
	v_med3_f32 v162, v162, s64, v159
	v_rcp_f32_e32 v166, v166
	v_rcp_f32_e32 v167, v167
	v_med3_f32 v163, v163, s64, v159
	v_pk_mul_f32 v[156:157], v[156:157], v[164:165]
	v_pk_fma_f32 v[160:161], v[26:27], s[24:25], v[152:153] op_sel_hi:[1,0,1]
	v_pk_mul_f32 v[156:157], v[162:163], v[156:157]
	v_pk_fma_f32 v[162:163], v[52:53], s[24:25], v[132:133] op_sel_hi:[1,0,1]
	v_med3_f32 v160, v160, s64, v159
	v_med3_f32 v161, v161, s64, v159
	v_pk_mul_f32 v[70:71], v[70:71], v[166:167]
	v_min_f32_e32 v162, 0x40e00000, v162
	v_pk_mul_f32 v[160:161], v[160:161], v[70:71]
	v_pk_fma_f32 v[70:71], v[54:55], s[24:25], v[134:135] op_sel_hi:[1,0,1]
	v_min_f32_e32 v163, 0x40e00000, v163
	v_mul_f32_e32 v1, 0xc01d265f, v162
	v_min_f32_e32 v168, 0x40e00000, v70
	v_exp_f32_e32 v70, v1
	v_mul_f32_e32 v1, 0xc01d265f, v163
	v_min_f32_e32 v169, 0x40e00000, v71
	v_exp_f32_e32 v71, v1
	v_mul_f32_e32 v1, 0xc01d265f, v168
	v_exp_f32_e32 v170, v1
	v_mul_f32_e32 v1, 0xc01d265f, v169
	v_exp_f32_e32 v171, v1
	v_pk_add_f32 v[70:71], v[70:71], 1.0 op_sel_hi:[1,0]
	v_pk_fma_f32 v[166:167], v[20:21], s[24:25], v[150:151] op_sel_hi:[1,0,1]
	v_rcp_f32_e32 v70, v70
	v_rcp_f32_e32 v71, v71
	v_pk_add_f32 v[170:171], v[170:171], 1.0 op_sel_hi:[1,0]
	v_med3_f32 v166, v166, s64, v159
	v_med3_f32 v167, v167, s64, v159
	v_rcp_f32_e32 v170, v170
	v_rcp_f32_e32 v171, v171
	v_pk_mul_f32 v[70:71], v[162:163], v[70:71]
	v_pk_fma_f32 v[164:165], v[22:23], s[24:25], v[148:149] op_sel_hi:[1,0,1]
	v_pk_mul_f32 v[162:163], v[166:167], v[70:71]
	v_mov_b32_e32 v70, 0
	v_mov_b32_e32 v71, 0
	v_cvt_pk_fp8_f32 v70, v156, v157
	v_cvt_pk_fp8_f32 v71, v162, v163
	v_med3_f32 v164, v164, s64, v159
	v_med3_f32 v165, v165, s64, v159
	v_pk_mul_f32 v[156:157], v[168:169], v[170:171]
	v_cvt_pk_fp8_f32 v70, v160, v161 op_sel:[0,0,1]
	v_pk_mul_f32 v[156:157], v[164:165], v[156:157]
	s_mov_b32 s5, 0x40000
	v_cvt_pk_fp8_f32 v71, v156, v157 op_sel:[0,0,1]
	v_add_co_u32_e32 v156, vcc, s5, v146
	v_permlane16_swap_b32_e32 v68, v70
	v_permlane16_swap_b32_e32 v69, v71
	v_addc_co_u32_e32 v157, vcc, 0, v147, vcc
	global_store_dwordx4 v[156:157], v[68:71], off
	v_pk_fma_f32 v[160:161], v[16:17], s[24:25], v[154:155] op_sel_hi:[1,0,1]
	v_pk_fma_f32 v[156:157], v[18:19], s[24:25], v[152:153] op_sel_hi:[1,0,1]
	v_pk_fma_f32 v[70:71], v[48:49], s[24:25], v[136:137] op_sel_hi:[1,0,1]
	v_pk_fma_f32 v[68:69], v[50:51], s[24:25], v[138:139] op_sel_hi:[1,0,1]
	v_min_f32_e32 v70, 0x40e00000, v70
	v_min_f32_e32 v71, 0x40e00000, v71
	v_mul_f32_e32 v1, 0xc01d265f, v70
	v_min_f32_e32 v68, 0x40e00000, v68
	v_exp_f32_e32 v162, v1
	v_mul_f32_e32 v1, 0xc01d265f, v71
	v_min_f32_e32 v69, 0x40e00000, v69
	v_mul_f32_e32 v141, 0xc01d265f, v68
	v_exp_f32_e32 v163, v1
	v_exp_f32_e32 v164, v141
	v_mul_f32_e32 v141, 0xc01d265f, v69
	v_exp_f32_e32 v165, v141
	v_pk_add_f32 v[162:163], v[162:163], 1.0 op_sel_hi:[1,0]
	v_med3_f32 v160, v160, s64, v159
	v_rcp_f32_e32 v162, v162
	v_rcp_f32_e32 v163, v163
	v_pk_add_f32 v[164:165], v[164:165], 1.0 op_sel_hi:[1,0]
	v_med3_f32 v161, v161, s64, v159
	v_rcp_f32_e32 v164, v164
	v_rcp_f32_e32 v165, v165
	v_pk_mul_f32 v[70:71], v[70:71], v[162:163]
	v_med3_f32 v156, v156, s64, v159
	v_pk_mul_f32 v[70:71], v[160:161], v[70:71]
	v_pk_fma_f32 v[160:161], v[44:45], s[24:25], v[132:133] op_sel_hi:[1,0,1]
	v_med3_f32 v157, v157, s64, v159
	v_pk_mul_f32 v[68:69], v[68:69], v[164:165]
	v_min_f32_e32 v160, 0x40e00000, v160
	v_pk_mul_f32 v[156:157], v[156:157], v[68:69]
	v_pk_fma_f32 v[68:69], v[46:47], s[24:25], v[134:135] op_sel_hi:[1,0,1]
	v_min_f32_e32 v161, 0x40e00000, v161
	v_mul_f32_e32 v1, 0xc01d265f, v160
	v_min_f32_e32 v166, 0x40e00000, v68
	v_exp_f32_e32 v68, v1
	v_mul_f32_e32 v1, 0xc01d265f, v161
	v_min_f32_e32 v167, 0x40e00000, v69
	v_exp_f32_e32 v69, v1
	v_mul_f32_e32 v1, 0xc01d265f, v166
	v_exp_f32_e32 v168, v1
	v_mul_f32_e32 v1, 0xc01d265f, v167
	v_exp_f32_e32 v169, v1
	v_pk_add_f32 v[68:69], v[68:69], 1.0 op_sel_hi:[1,0]
	v_pk_fma_f32 v[164:165], v[12:13], s[24:25], v[150:151] op_sel_hi:[1,0,1]
	v_rcp_f32_e32 v68, v68
	v_rcp_f32_e32 v69, v69
	v_pk_add_f32 v[168:169], v[168:169], 1.0 op_sel_hi:[1,0]
	v_med3_f32 v164, v164, s64, v159
	v_med3_f32 v165, v165, s64, v159
	v_rcp_f32_e32 v168, v168
	v_rcp_f32_e32 v169, v169
	v_pk_mul_f32 v[68:69], v[160:161], v[68:69]
	v_pk_fma_f32 v[162:163], v[14:15], s[24:25], v[148:149] op_sel_hi:[1,0,1]
	v_pk_mul_f32 v[160:161], v[164:165], v[68:69]
	v_mov_b32_e32 v69, 0
	v_cvt_pk_fp8_f32 v69, v160, v161
	v_mov_b32_e32 v68, 0
	v_med3_f32 v162, v162, s64, v159
	v_med3_f32 v163, v163, s64, v159
	v_cvt_pk_fp8_f32 v68, v70, v71
	v_pk_mul_f32 v[70:71], v[166:167], v[168:169]
	v_pk_fma_f32 v[136:137], v[40:41], s[24:25], v[136:137] op_sel_hi:[1,0,1]
	v_pk_mul_f32 v[70:71], v[162:163], v[70:71]
	v_cvt_pk_fp8_f32 v68, v156, v157 op_sel:[0,0,1]
	v_cvt_pk_fp8_f32 v69, v70, v71 op_sel:[0,0,1]
	v_pk_fma_f32 v[70:71], v[42:43], s[24:25], v[138:139] op_sel_hi:[1,0,1]
	v_min_f32_e32 v136, 0x40e00000, v136
	v_min_f32_e32 v70, 0x40e00000, v70
	v_min_f32_e32 v71, 0x40e00000, v71
	v_mul_f32_e32 v141, 0xc01d265f, v70
	v_exp_f32_e32 v156, v141
	v_mul_f32_e32 v141, 0xc01d265f, v71
	v_exp_f32_e32 v157, v141
	v_min_f32_e32 v137, 0x40e00000, v137
	v_mul_f32_e32 v1, 0xc01d265f, v136
	v_pk_fma_f32 v[138:139], v[10:11], s[24:25], v[152:153] op_sel_hi:[1,0,1]
	v_pk_fma_f32 v[152:153], v[8:9], s[24:25], v[154:155] op_sel_hi:[1,0,1]
	v_exp_f32_e32 v154, v1
	v_mul_f32_e32 v1, 0xc01d265f, v137
	v_pk_add_f32 v[156:157], v[156:157], 1.0 op_sel_hi:[1,0]
	v_exp_f32_e32 v155, v1
	v_rcp_f32_e32 v156, v156
	v_rcp_f32_e32 v157, v157
	v_pk_fma_f32 v[132:133], v[36:37], s[24:25], v[132:133] op_sel_hi:[1,0,1]
	v_pk_add_f32 v[154:155], v[154:155], 1.0 op_sel_hi:[1,0]
	v_med3_f32 v138, v138, s64, v159
	v_med3_f32 v139, v139, s64, v159
	v_pk_mul_f32 v[70:71], v[70:71], v[156:157]
	v_min_f32_e32 v132, 0x40e00000, v132
	v_rcp_f32_e32 v154, v154
	v_rcp_f32_e32 v155, v155
	v_pk_mul_f32 v[138:139], v[138:139], v[70:71]
	v_pk_fma_f32 v[70:71], v[38:39], s[24:25], v[134:135] op_sel_hi:[1,0,1]
	v_min_f32_e32 v133, 0x40e00000, v133
	v_mul_f32_e32 v1, 0xc01d265f, v132
	v_pk_fma_f32 v[134:135], v[6:7], s[24:25], v[148:149] op_sel_hi:[1,0,1]
	v_pk_fma_f32 v[148:149], v[4:5], s[24:25], v[150:151] op_sel_hi:[1,0,1]
	v_min_f32_e32 v150, 0x40e00000, v70
	v_exp_f32_e32 v70, v1
	v_mul_f32_e32 v1, 0xc01d265f, v133
	v_min_f32_e32 v151, 0x40e00000, v71
	v_exp_f32_e32 v71, v1
	v_med3_f32 v152, v152, s64, v159
	v_med3_f32 v153, v153, s64, v159
	v_pk_mul_f32 v[136:137], v[136:137], v[154:155]
	v_mul_f32_e32 v1, 0xc01d265f, v150
	v_pk_mul_f32 v[136:137], v[152:153], v[136:137]
	v_exp_f32_e32 v152, v1
	v_mul_f32_e32 v1, 0xc01d265f, v151
	v_exp_f32_e32 v153, v1
	v_pk_add_f32 v[70:71], v[70:71], 1.0 op_sel_hi:[1,0]
	v_med3_f32 v148, v148, s64, v159
	v_rcp_f32_e32 v70, v70
	v_rcp_f32_e32 v71, v71
	v_pk_add_f32 v[152:153], v[152:153], 1.0 op_sel_hi:[1,0]
	v_med3_f32 v149, v149, s64, v159
	v_rcp_f32_e32 v152, v152
	v_rcp_f32_e32 v153, v153
	v_pk_mul_f32 v[70:71], v[132:133], v[70:71]
	v_med3_f32 v134, v134, s64, v159
	v_pk_mul_f32 v[132:133], v[148:149], v[70:71]
	v_mov_b32_e32 v70, 0
	v_mov_b32_e32 v71, 0
	v_cvt_pk_fp8_f32 v70, v136, v137
	v_cvt_pk_fp8_f32 v71, v132, v133
	v_med3_f32 v135, v135, s64, v159
	v_pk_mul_f32 v[132:133], v[150:151], v[152:153]
	v_cvt_pk_fp8_f32 v70, v138, v139 op_sel:[0,0,1]
	v_pk_mul_f32 v[132:133], v[134:135], v[132:133]
	s_nop 0
	v_permlane16_swap_b32_e32 v68, v70
	v_cvt_pk_fp8_f32 v71, v132, v133 op_sel:[0,0,1]
	v_add_co_u32_e32 v132, vcc, 0x50000, v146
	s_nop 0
	v_permlane16_swap_b32_e32 v69, v71
	v_addc_co_u32_e32 v133, vcc, 0, v147, vcc
	s_andn2_b64 vcc, exec, s[36:37]
	global_store_dwordx4 v[132:133], v[68:71], off
	s_cbranch_vccnz .LBB0_803
	s_waitcnt vmcnt(4)
	v_xor_b32_e32 v204, 0x400, v204
	ds_write_b128 v204, v[184:187]
	ds_write_b128 v204, v[188:191] offset:16
	ds_write_b128 v204, v[192:195] offset:512
	ds_write_b128 v204, v[196:199] offset:528
	ds_read_b128 v[0:3], v253
	s_andn2_b64 vcc, exec, s[20:21]
	s_cbranch_vccnz .LBB0_802
	s_barrier
	s_branch .LBB0_802

.LBB0_886:
	v_and_b32_e32 v5, 15, v4
	s_add_i32 s0, 0, 0x21000
	v_or_b32_e32 v6, s53, v5
	v_lshl_add_u32 v253, v4, 4, s0
	v_and_b32_e32 v7, 48, v4
	v_lshlrev_b32_e32 v8, 6, v6
	s_movk_i32 s0, 0x3c0
	v_and_or_b32 v8, v8, s0, v7
	v_lshlrev_b32_e32 v4, 2, v4
	s_add_u32 s0, s18, 0x80
	v_lshl_or_b32 v5, v5, 6, v7
	v_and_b32_e32 v4, 32, v4
	s_addc_u32 s1, s19, 0
	v_bitop3_b32 v158, v5, s56, v4 bitop3:0xde
	s_waitcnt vmcnt(2)
	s_barrier
	s_add_i32 m0, s7, 0x18000
	v_lshl_add_u64 v[4:5], s[0:1], 0, v[140:141]
	v_lshlrev_b32_e32 v6, 2, v6
	global_load_lds_dwordx4 v[4:5], off
	s_add_i32 m0, s7, 0x1a000
	v_and_b32_e32 v6, 32, v6
	v_lshl_add_u64 v[4:5], s[0:1], 0, v[142:143]
	s_add_u32 s0, s90, 0x12800080
	v_bitop3_b32 v6, v8, s55, v6 bitop3:0xde
	s_addc_u32 s1, s91, 0
	s_add_i32 s55, s7, 0x8000
	global_load_lds_dwordx4 v[4:5], off
	s_mov_b32 m0, s55
	v_lshl_add_u64 v[4:5], s[0:1], 0, v[0:1]
	s_add_i32 s56, s7, 0xa000
	global_load_lds_dwordx4 v[4:5], off
	v_lshl_add_u64 v[4:5], s[0:1], 0, v[144:145]
	s_add_u32 s0, s18, 0x40080
	s_mov_b32 m0, s56
	s_addc_u32 s1, s19, 0
	global_load_lds_dwordx4 v[4:5], off
	s_add_i32 m0, s7, 0x1c000
	v_lshl_add_u64 v[4:5], s[0:1], 0, v[140:141]
	global_load_lds_dwordx4 v[4:5], off
	v_lshl_add_u64 v[4:5], s[0:1], 0, v[142:143]
	s_add_i32 m0, s7, 0x1e000
	v_readlane_b32 s0, v255, 25
	global_load_lds_dwordx4 v[4:5], off
	s_waitcnt vmcnt(6)
	s_cmpk_lt_u32 s0, 0x100
	s_cselect_b64 s[22:23], -1, 0
	s_add_i32 s57, 0, 0x10000
	s_add_i32 s61, 0, 0x14000
	v_add_u32_e32 v143, 0, v6
	v_mov_b32_e32 v145, 0x7f7f7f7f
	s_mov_b32 s24, 0x3c800000
	s_mov_b32 s62, 0xc0c00000
	s_mov_b32 s63, 0x40000
	v_mov_b32_e32 v159, 0x41000000
	v_mov_b32_e32 v4, v141
	v_mov_b32_e32 v5, v141
	v_mov_b32_e32 v6, v141
	v_mov_b32_e32 v7, v141
	v_mov_b32_e32 v8, v141
	v_mov_b32_e32 v9, v141
	v_mov_b32_e32 v10, v141
	v_mov_b32_e32 v11, v141
	s_waitcnt vmcnt(0)
	v_mov_b32_e32 v12, v141
	v_mov_b32_e32 v13, v141
	v_mov_b32_e32 v14, v141
	v_mov_b32_e32 v15, v141
	v_mov_b32_e32 v16, v141
	v_mov_b32_e32 v17, v141
	v_mov_b32_e32 v18, v141
	v_mov_b32_e32 v19, v141
	v_mov_b32_e32 v20, v141
	v_mov_b32_e32 v21, v141
	v_mov_b32_e32 v22, v141
	v_mov_b32_e32 v23, v141
	v_mov_b32_e32 v24, v141
	v_mov_b32_e32 v25, v141
	v_mov_b32_e32 v26, v141
	v_mov_b32_e32 v27, v141
	v_mov_b32_e32 v232, v141
	v_mov_b32_e32 v233, v141
	v_mov_b32_e32 v234, v141
	v_mov_b32_e32 v235, v141
	v_mov_b32_e32 v32, v141
	v_mov_b32_e32 v33, v141
	v_mov_b32_e32 v34, v141
	v_mov_b32_e32 v35, v141
	v_mov_b32_e32 v36, v141
	v_mov_b32_e32 v37, v141
	v_mov_b32_e32 v38, v141
	v_mov_b32_e32 v39, v141
	v_mov_b32_e32 v40, v141
	v_mov_b32_e32 v41, v141
	v_mov_b32_e32 v42, v141
	v_mov_b32_e32 v43, v141
	v_mov_b32_e32 v44, v141
	v_mov_b32_e32 v45, v141
	v_mov_b32_e32 v46, v141
	v_mov_b32_e32 v47, v141
	v_mov_b32_e32 v48, v141
	v_mov_b32_e32 v49, v141
	v_mov_b32_e32 v50, v141
	v_mov_b32_e32 v51, v141
	v_mov_b32_e32 v52, v141
	v_mov_b32_e32 v53, v141
	v_mov_b32_e32 v54, v141
	v_mov_b32_e32 v55, v141
	v_mov_b32_e32 v56, v141
	v_mov_b32_e32 v57, v141
	v_mov_b32_e32 v58, v141
	v_mov_b32_e32 v59, v141
	v_mov_b32_e32 v60, v141
	v_mov_b32_e32 v61, v141
	v_mov_b32_e32 v62, v141
	v_mov_b32_e32 v63, v141
	v_mov_b32_e32 v64, v141
	v_mov_b32_e32 v65, v141
	v_mov_b32_e32 v66, v141
	v_mov_b32_e32 v67, v141
	v_mov_b32_e32 v28, v141
	v_mov_b32_e32 v29, v141
	v_mov_b32_e32 v30, v141
	v_mov_b32_e32 v31, v141
	v_mov_b32_e32 v72, v141
	v_mov_b32_e32 v73, v141
	v_mov_b32_e32 v74, v141
	v_mov_b32_e32 v75, v141
	v_mov_b32_e32 v76, v141
	v_mov_b32_e32 v77, v141
	v_mov_b32_e32 v78, v141
	v_mov_b32_e32 v79, v141
	v_mov_b32_e32 v80, v141
	v_mov_b32_e32 v81, v141
	v_mov_b32_e32 v82, v141
	v_mov_b32_e32 v83, v141
	v_mov_b32_e32 v84, v141
	v_mov_b32_e32 v85, v141
	v_mov_b32_e32 v86, v141
	v_mov_b32_e32 v87, v141
	v_mov_b32_e32 v88, v141
	v_mov_b32_e32 v89, v141
	v_mov_b32_e32 v90, v141
	v_mov_b32_e32 v91, v141
	v_mov_b32_e32 v92, v141
	v_mov_b32_e32 v93, v141
	v_mov_b32_e32 v94, v141
	v_mov_b32_e32 v95, v141
	v_mov_b32_e32 v96, v141
	v_mov_b32_e32 v97, v141
	v_mov_b32_e32 v98, v141
	v_mov_b32_e32 v99, v141
	v_mov_b32_e32 v100, v141
	v_mov_b32_e32 v101, v141
	v_mov_b32_e32 v102, v141
	v_mov_b32_e32 v103, v141
	v_mov_b32_e32 v104, v141
	v_mov_b32_e32 v105, v141
	v_mov_b32_e32 v106, v141
	v_mov_b32_e32 v107, v141
	v_mov_b32_e32 v108, v141
	v_mov_b32_e32 v109, v141
	v_mov_b32_e32 v110, v141
	v_mov_b32_e32 v111, v141
	v_mov_b32_e32 v112, v141
	v_mov_b32_e32 v113, v141
	v_mov_b32_e32 v114, v141
	v_mov_b32_e32 v115, v141
	v_mov_b32_e32 v116, v141
	v_mov_b32_e32 v117, v141
	v_mov_b32_e32 v118, v141
	v_mov_b32_e32 v119, v141
	v_mov_b32_e32 v120, v141
	v_mov_b32_e32 v121, v141
	v_mov_b32_e32 v122, v141
	v_mov_b32_e32 v123, v141
	v_mov_b32_e32 v124, v141
	v_mov_b32_e32 v125, v141
	v_mov_b32_e32 v126, v141
	v_mov_b32_e32 v127, v141
	v_mov_b32_e32 v128, v141
	v_mov_b32_e32 v129, v141
	v_mov_b32_e32 v130, v141
	v_mov_b32_e32 v131, v141
	s_barrier
	v_mbcnt_lo_u32_b32 v200, -1, 0
	v_mbcnt_hi_u32_b32 v200, -1, v200
	v_lshrrev_b32_e32 v200, 4, v200
	v_readlane_b32 s98, v255, 35
	v_readlane_b32 s99, v255, 36
	v_readlane_b32 s100, v255, 39
	v_readlane_b32 s101, v255, 40
	s_lshl_b32 vcc_lo, s4, 13
	s_add_u32 s98, s98, vcc_lo
	s_addc_u32 s99, s99, 0
	s_add_u32 s100, s100, vcc_lo
	s_addc_u32 s101, s101, 0
	s_lshl_b32 vcc_lo, s6, 7
	s_or_b32 vcc_lo, vcc_lo, s54
	v_lshl_add_u32 v201, v200, 3, vcc_lo
	v_lshlrev_b32_e32 v201, 2, v201
	global_load_dwordx4 v[184:187], v201, s[98:99]
	global_load_dwordx4 v[188:191], v201, s[98:99] offset:16
	global_load_dwordx4 v[192:195], v201, s[100:101]
	global_load_dwordx4 v[196:199], v201, s[100:101] offset:16
	v_lshl_add_u32 v204, v200, 3, s54
	v_lshlrev_b32_e32 v204, 2, v204
	s_and_b32 vcc_lo, s60, 1
	s_lshl_b32 vcc_lo, vcc_lo, 10
	s_add_u32 vcc_lo, vcc_lo, 0x26800
	v_add_u32_e32 v204, vcc_lo, v204
	s_waitcnt vmcnt(0)
	ds_write_b128 v204, v[184:187]
	ds_write_b128 v204, v[188:191] offset:16
	ds_write_b128 v204, v[192:195] offset:512
	ds_write_b128 v204, v[196:199] offset:528
	s_branch .LBB0_889

.LBB0_922:
	s_lshl_b32 s5, s6, 7
	v_mbcnt_lo_u32_b32 v1, -1, 0
	v_mbcnt_hi_u32_b32 v1, -1, v1
	s_or_b32 s5, s5, s54
	v_ashrrev_i32_e32 v141, 4, v1
	v_lshl_add_u32 v146, v141, 3, s5
	s_ashr_i32 s5, s4, 31
	v_readlane_b32 s72, v255, 31
	s_lshl_b64 s[38:39], s[4:5], 13
	v_readlane_b32 s76, v255, 35
	v_readlane_b32 s77, v255, 36
	s_add_u32 s40, s76, s38
	v_readlane_b32 s80, v255, 39
	s_addc_u32 s41, s77, s39
	v_ashrrev_i32_e32 v147, 31, v146
	v_readlane_b32 s81, v255, 40
	v_lshlrev_b64 v[68:69], 2, v[146:147]
	s_add_u32 s38, s80, s38
	v_lshl_add_u64 v[70:71], s[40:41], 0, v[68:69]
	s_addc_u32 s39, s81, s39
	s_lshl_b32 s98, s6, 7
	v_subrev_u32_e32 v204, s98, v146
	v_lshlrev_b32_e32 v204, 2, v204
	s_and_b32 s99, s60, 1
	s_lshl_b32 s99, s99, 10
	s_add_u32 s99, s99, 0x26800
	v_add_u32_e32 v204, s99, v204
	ds_read_b128 v[136:139], v204
	ds_read_b128 v[132:135], v204 offset:16
	v_lshl_add_u64 v[148:149], s[38:39], 0, v[68:69]
	ds_read_b128 v[68:71], v204 offset:512
	ds_read_b128 v[160:163], v204 offset:528
	s_cmp_lg_u32 s36, 0
	s_cbranch_scc0 .Lnb_skip_p6b
	s_lshl_b32 s98, s28, 7
	s_or_b32 s98, s98, s54
	v_lshl_add_u32 v200, v141, 3, s98
	v_lshlrev_b32_e32 v200, 2, v200
	s_lshl_b32 s98, s26, 13
	s_add_u32 s100, s80, s98
	s_addc_u32 s101, s81, 0
	s_add_u32 s98, s76, s98
	s_addc_u32 s99, s77, 0
	global_load_dwordx4 v[184:187], v200, s[98:99]
	global_load_dwordx4 v[188:191], v200, s[98:99] offset:16
	global_load_dwordx4 v[192:195], v200, s[100:101]
	global_load_dwordx4 v[196:199], v200, s[100:101] offset:16
.Lnb_skip_p6b:
	v_and_b32_e32 v141, 1, v141
	v_and_b32_e32 v1, 15, v1
	v_lshlrev_b32_e32 v150, 4, v141
	s_add_i32 s5, s2, s53
	v_add3_u32 v150, s5, v1, v150
	v_ashrrev_i32_e32 v151, 31, v150
	v_lshlrev_b32_e32 v141, 3, v141
	v_lshlrev_b64 v[150:151], 11, v[150:151]
	v_sub_co_u32_e32 v148, vcc, 0, v141
	v_lshl_add_u64 v[150:151], s[14:15], 0, v[150:151]
	v_lshl_add_u64 v[146:147], v[150:151], 0, v[146:147]
	v_subb_co_u32_e64 v149, s[38:39], 0, 0, vcc
	v_lshl_add_u64 v[146:147], v[146:147], 0, v[148:149]
	v_mov_b32_e32 v164, 0
	v_mov_b32_e32 v165, 0
	v_readlane_b32 s73, v255, 32
	v_readlane_b32 s74, v255, 33
	v_readlane_b32 s75, v255, 34
	v_readlane_b32 s78, v255, 37
	v_readlane_b32 s79, v255, 38
	v_readlane_b32 s82, v255, 41
	v_readlane_b32 s83, v255, 42
	v_readlane_b32 s84, v255, 43
	v_readlane_b32 s85, v255, 44
	v_readlane_b32 s86, v255, 45
	v_readlane_b32 s87, v255, 46
	s_waitcnt lgkmcnt(0)
	v_pk_fma_f32 v[166:167], v[128:129], s[24:25], v[136:137] op_sel_hi:[1,0,1]
	v_pk_fma_f32 v[156:157], v[130:131], s[24:25], v[138:139] op_sel_hi:[1,0,1]
	v_pk_add_f32 v[154:155], v[68:69], 1.0 op_sel_hi:[1,0]
	v_min_f32_e32 v68, 0x40e00000, v166
	v_min_f32_e32 v69, 0x40e00000, v167
	v_pk_fma_f32 v[168:169], v[126:127], s[24:25], v[134:135] op_sel_hi:[1,0,1]
	v_mul_f32_e32 v1, 0xc01d265f, v68
	v_mul_f32_e32 v141, 0xc01d265f, v69
	v_pk_add_f32 v[152:153], v[70:71], 1.0 op_sel_hi:[1,0]
	v_pk_add_f32 v[150:151], v[160:161], 1.0 op_sel_hi:[1,0]
	v_min_f32_e32 v70, 0x40e00000, v156
	v_min_f32_e32 v71, 0x40e00000, v157
	v_min_f32_e32 v160, 0x40e00000, v168
	v_min_f32_e32 v161, 0x40e00000, v169
	v_exp_f32_e32 v174, v1
	v_exp_f32_e32 v175, v141
	v_mul_f32_e32 v176, 0xc01d265f, v70
	v_mul_f32_e32 v177, 0xc01d265f, v71
	v_mul_f32_e32 v180, 0xc01d265f, v160
	v_mul_f32_e32 v181, 0xc01d265f, v161
	v_exp_f32_e32 v176, v176
	v_exp_f32_e32 v177, v177
	v_exp_f32_e32 v180, v180
	v_exp_f32_e32 v181, v181
	v_pk_add_f32 v[174:175], v[174:175], 1.0 op_sel_hi:[1,0]
	v_pk_fma_f32 v[170:171], v[124:125], s[24:25], v[132:133] op_sel_hi:[1,0,1]
	v_rcp_f32_e32 v174, v174
	v_rcp_f32_e32 v175, v175
	v_min_f32_e32 v156, 0x40e00000, v170
	v_min_f32_e32 v157, 0x40e00000, v171
	v_pk_add_f32 v[176:177], v[176:177], 1.0 op_sel_hi:[1,0]
	v_pk_add_f32 v[180:181], v[180:181], 1.0 op_sel_hi:[1,0]
	v_mul_f32_e32 v178, 0xc01d265f, v156
	v_mul_f32_e32 v179, 0xc01d265f, v157
	v_rcp_f32_e32 v176, v176
	v_rcp_f32_e32 v177, v177
	v_rcp_f32_e32 v180, v180
	v_rcp_f32_e32 v181, v181
	v_pk_fma_f32 v[166:167], v[96:97], s[24:25], v[154:155] op_sel_hi:[1,0,1]
	v_exp_f32_e32 v178, v178
	v_exp_f32_e32 v179, v179
	v_pk_add_f32 v[148:149], v[162:163], 1.0 op_sel_hi:[1,0]
	v_med3_f32 v166, v166, s62, v159
	v_med3_f32 v167, v167, s62, v159
	v_pk_mul_f32 v[68:69], v[68:69], v[174:175]
	v_pk_fma_f32 v[162:163], v[98:99], s[24:25], v[152:153] op_sel_hi:[1,0,1]
	v_pk_fma_f32 v[168:169], v[94:95], s[24:25], v[148:149] op_sel_hi:[1,0,1]
	v_pk_mul_f32 v[68:69], v[166:167], v[68:69]
	v_pk_fma_f32 v[172:173], v[122:123], s[24:25], v[138:139] op_sel_hi:[1,0,1]
	v_med3_f32 v162, v162, s62, v159
	v_med3_f32 v163, v163, s62, v159
	v_med3_f32 v168, v168, s62, v159
	v_med3_f32 v169, v169, s62, v159
	v_pk_mul_f32 v[70:71], v[70:71], v[176:177]
	v_pk_mul_f32 v[160:161], v[160:161], v[180:181]
	v_cvt_pk_fp8_f32 v164, v68, v69
	v_pk_add_f32 v[178:179], v[178:179], 1.0 op_sel_hi:[1,0]
	v_pk_mul_f32 v[68:69], v[162:163], v[70:71]
	v_pk_mul_f32 v[70:71], v[168:169], v[160:161]
	v_min_f32_e32 v160, 0x40e00000, v172
	v_rcp_f32_e32 v178, v178
	v_rcp_f32_e32 v179, v179
	v_min_f32_e32 v161, 0x40e00000, v173
	v_mul_f32_e32 v141, 0xc01d265f, v160
	v_exp_f32_e32 v166, v141
	v_mul_f32_e32 v141, 0xc01d265f, v161
	v_cvt_pk_fp8_f32 v164, v68, v69 op_sel:[0,0,1]
	v_pk_fma_f32 v[68:69], v[120:121], s[24:25], v[136:137] op_sel_hi:[1,0,1]
	v_exp_f32_e32 v167, v141
	v_pk_fma_f32 v[170:171], v[92:93], s[24:25], v[150:151] op_sel_hi:[1,0,1]
	v_min_f32_e32 v68, 0x40e00000, v68
	v_med3_f32 v170, v170, s62, v159
	v_med3_f32 v171, v171, s62, v159
	v_pk_mul_f32 v[156:157], v[156:157], v[178:179]
	v_min_f32_e32 v69, 0x40e00000, v69
	v_mul_f32_e32 v1, 0xc01d265f, v68
	v_pk_mul_f32 v[156:157], v[170:171], v[156:157]
	v_exp_f32_e32 v162, v1
	v_mul_f32_e32 v1, 0xc01d265f, v69
	v_cvt_pk_fp8_f32 v165, v156, v157
	v_exp_f32_e32 v163, v1
	v_pk_add_f32 v[166:167], v[166:167], 1.0 op_sel_hi:[1,0]
	v_pk_fma_f32 v[156:157], v[88:89], s[24:25], v[154:155] op_sel_hi:[1,0,1]
	v_rcp_f32_e32 v166, v166
	v_rcp_f32_e32 v167, v167
	v_cvt_pk_fp8_f32 v165, v70, v71 op_sel:[0,0,1]
	v_pk_fma_f32 v[70:71], v[90:91], s[24:25], v[152:153] op_sel_hi:[1,0,1]
	v_pk_add_f32 v[162:163], v[162:163], 1.0 op_sel_hi:[1,0]
	v_med3_f32 v70, v70, s62, v159
	v_rcp_f32_e32 v162, v162
	v_rcp_f32_e32 v163, v163
	v_med3_f32 v71, v71, s62, v159
	v_pk_mul_f32 v[160:161], v[160:161], v[166:167]
	v_med3_f32 v156, v156, s62, v159
	v_pk_mul_f32 v[70:71], v[70:71], v[160:161]
	v_pk_fma_f32 v[160:161], v[116:117], s[24:25], v[132:133] op_sel_hi:[1,0,1]
	v_med3_f32 v157, v157, s62, v159
	v_min_f32_e32 v160, 0x40e00000, v160
	v_min_f32_e32 v161, 0x40e00000, v161
	v_mul_f32_e32 v1, 0xc01d265f, v160
	v_pk_mul_f32 v[68:69], v[68:69], v[162:163]
	v_exp_f32_e32 v168, v1
	v_mul_f32_e32 v1, 0xc01d265f, v161
	v_pk_mul_f32 v[68:69], v[156:157], v[68:69]
	v_pk_fma_f32 v[156:157], v[118:119], s[24:25], v[134:135] op_sel_hi:[1,0,1]
	v_exp_f32_e32 v169, v1
	v_min_f32_e32 v156, 0x40e00000, v156
	v_min_f32_e32 v157, 0x40e00000, v157
	v_mul_f32_e32 v1, 0xc01d265f, v156
	v_exp_f32_e32 v170, v1
	v_mul_f32_e32 v1, 0xc01d265f, v157
	v_exp_f32_e32 v171, v1
	v_pk_add_f32 v[168:169], v[168:169], 1.0 op_sel_hi:[1,0]
	v_pk_fma_f32 v[166:167], v[84:85], s[24:25], v[150:151] op_sel_hi:[1,0,1]
	v_rcp_f32_e32 v168, v168
	v_rcp_f32_e32 v169, v169
	v_pk_add_f32 v[170:171], v[170:171], 1.0 op_sel_hi:[1,0]
	v_med3_f32 v166, v166, s62, v159
	v_med3_f32 v167, v167, s62, v159
	v_rcp_f32_e32 v170, v170
	v_rcp_f32_e32 v171, v171
	v_pk_mul_f32 v[160:161], v[160:161], v[168:169]
	v_pk_fma_f32 v[162:163], v[86:87], s[24:25], v[148:149] op_sel_hi:[1,0,1]
	v_pk_mul_f32 v[160:161], v[166:167], v[160:161]
	v_mov_b32_e32 v166, 0
	v_mov_b32_e32 v167, 0
	v_cvt_pk_fp8_f32 v166, v68, v69
	v_cvt_pk_fp8_f32 v167, v160, v161
	v_med3_f32 v162, v162, s62, v159
	v_med3_f32 v163, v163, s62, v159
	v_pk_mul_f32 v[68:69], v[156:157], v[170:171]
	v_cvt_pk_fp8_f32 v166, v70, v71 op_sel:[0,0,1]
	v_pk_mul_f32 v[68:69], v[162:163], v[68:69]
	v_pk_fma_f32 v[70:71], v[112:113], s[24:25], v[136:137] op_sel_hi:[1,0,1]
	v_cvt_pk_fp8_f32 v167, v68, v69 op_sel:[0,0,1]
	v_min_f32_e32 v70, 0x40e00000, v70
	v_pk_fma_f32 v[68:69], v[114:115], s[24:25], v[138:139] op_sel_hi:[1,0,1]
	v_min_f32_e32 v71, 0x40e00000, v71
	v_mul_f32_e32 v1, 0xc01d265f, v70
	v_min_f32_e32 v68, 0x40e00000, v68
	v_exp_f32_e32 v162, v1
	v_mul_f32_e32 v1, 0xc01d265f, v71
	v_permlane16_swap_b32_e32 v164, v166
	v_permlane16_swap_b32_e32 v165, v167
	v_min_f32_e32 v69, 0x40e00000, v69
	v_mul_f32_e32 v141, 0xc01d265f, v68
	v_exp_f32_e32 v163, v1
	global_store_dwordx4 v[146:147], v[164:167], off
	v_pk_fma_f32 v[160:161], v[80:81], s[24:25], v[154:155] op_sel_hi:[1,0,1]
	v_pk_fma_f32 v[156:157], v[82:83], s[24:25], v[152:153] op_sel_hi:[1,0,1]
	v_exp_f32_e32 v164, v141
	v_mul_f32_e32 v141, 0xc01d265f, v69
	v_exp_f32_e32 v165, v141
	v_pk_add_f32 v[162:163], v[162:163], 1.0 op_sel_hi:[1,0]
	v_med3_f32 v160, v160, s62, v159
	v_rcp_f32_e32 v162, v162
	v_rcp_f32_e32 v163, v163
	v_pk_add_f32 v[164:165], v[164:165], 1.0 op_sel_hi:[1,0]
	v_med3_f32 v161, v161, s62, v159
	v_rcp_f32_e32 v164, v164
	v_rcp_f32_e32 v165, v165
	v_pk_mul_f32 v[70:71], v[70:71], v[162:163]
	v_med3_f32 v156, v156, s62, v159
	v_pk_mul_f32 v[70:71], v[160:161], v[70:71]
	v_pk_fma_f32 v[160:161], v[108:109], s[24:25], v[132:133] op_sel_hi:[1,0,1]
	v_med3_f32 v157, v157, s62, v159
	v_pk_mul_f32 v[68:69], v[68:69], v[164:165]
	v_min_f32_e32 v160, 0x40e00000, v160
	v_pk_mul_f32 v[156:157], v[156:157], v[68:69]
	v_pk_fma_f32 v[68:69], v[110:111], s[24:25], v[134:135] op_sel_hi:[1,0,1]
	v_min_f32_e32 v161, 0x40e00000, v161
	v_mul_f32_e32 v1, 0xc01d265f, v160
	v_min_f32_e32 v166, 0x40e00000, v68
	v_exp_f32_e32 v68, v1
	v_mul_f32_e32 v1, 0xc01d265f, v161
	v_min_f32_e32 v167, 0x40e00000, v69
	v_exp_f32_e32 v69, v1
	v_mul_f32_e32 v1, 0xc01d265f, v166
	v_exp_f32_e32 v168, v1
	v_mul_f32_e32 v1, 0xc01d265f, v167
	v_pk_add_f32 v[68:69], v[68:69], 1.0 op_sel_hi:[1,0]
	v_exp_f32_e32 v169, v1
	v_rcp_f32_e32 v68, v68
	v_rcp_f32_e32 v69, v69
	v_pk_fma_f32 v[164:165], v[76:77], s[24:25], v[150:151] op_sel_hi:[1,0,1]
	v_pk_add_f32 v[168:169], v[168:169], 1.0 op_sel_hi:[1,0]
	v_med3_f32 v164, v164, s62, v159
	v_med3_f32 v165, v165, s62, v159
	v_pk_mul_f32 v[68:69], v[160:161], v[68:69]
	v_rcp_f32_e32 v168, v168
	v_pk_mul_f32 v[160:161], v[164:165], v[68:69]
	v_mov_b32_e32 v68, 0
	v_rcp_f32_e32 v169, v169
	v_cvt_pk_fp8_f32 v68, v70, v71
	v_mov_b32_e32 v69, 0
	v_cvt_pk_fp8_f32 v69, v160, v161
	v_pk_fma_f32 v[162:163], v[78:79], s[24:25], v[148:149] op_sel_hi:[1,0,1]
	v_pk_mul_f32 v[70:71], v[166:167], v[168:169]
	v_med3_f32 v162, v162, s62, v159
	v_med3_f32 v163, v163, s62, v159
	v_cvt_pk_fp8_f32 v68, v156, v157 op_sel:[0,0,1]
	v_pk_fma_f32 v[156:157], v[104:105], s[24:25], v[136:137] op_sel_hi:[1,0,1]
	v_pk_mul_f32 v[70:71], v[162:163], v[70:71]
	v_min_f32_e32 v156, 0x40e00000, v156
	v_cvt_pk_fp8_f32 v69, v70, v71 op_sel:[0,0,1]
	v_pk_fma_f32 v[70:71], v[106:107], s[24:25], v[138:139] op_sel_hi:[1,0,1]
	v_min_f32_e32 v157, 0x40e00000, v157
	v_mul_f32_e32 v1, 0xc01d265f, v156
	v_min_f32_e32 v70, 0x40e00000, v70
	v_exp_f32_e32 v164, v1
	v_mul_f32_e32 v1, 0xc01d265f, v157
	v_min_f32_e32 v71, 0x40e00000, v71
	v_mul_f32_e32 v141, 0xc01d265f, v70
	v_exp_f32_e32 v165, v1
	v_exp_f32_e32 v166, v141
	v_mul_f32_e32 v141, 0xc01d265f, v71
	v_exp_f32_e32 v167, v141
	v_pk_add_f32 v[164:165], v[164:165], 1.0 op_sel_hi:[1,0]
	v_pk_fma_f32 v[162:163], v[72:73], s[24:25], v[154:155] op_sel_hi:[1,0,1]
	v_rcp_f32_e32 v164, v164
	v_rcp_f32_e32 v165, v165
	v_pk_add_f32 v[166:167], v[166:167], 1.0 op_sel_hi:[1,0]
	v_med3_f32 v162, v162, s62, v159
	v_rcp_f32_e32 v166, v166
	v_rcp_f32_e32 v167, v167
	v_med3_f32 v163, v163, s62, v159
	v_pk_mul_f32 v[156:157], v[156:157], v[164:165]
	v_pk_fma_f32 v[160:161], v[74:75], s[24:25], v[152:153] op_sel_hi:[1,0,1]
	v_pk_mul_f32 v[156:157], v[162:163], v[156:157]
	v_pk_fma_f32 v[162:163], v[100:101], s[24:25], v[132:133] op_sel_hi:[1,0,1]
	v_med3_f32 v160, v160, s62, v159
	v_med3_f32 v161, v161, s62, v159
	v_pk_mul_f32 v[70:71], v[70:71], v[166:167]
	v_min_f32_e32 v162, 0x40e00000, v162
	v_pk_mul_f32 v[160:161], v[160:161], v[70:71]
	v_pk_fma_f32 v[70:71], v[102:103], s[24:25], v[134:135] op_sel_hi:[1,0,1]
	v_min_f32_e32 v163, 0x40e00000, v163
	v_mul_f32_e32 v1, 0xc01d265f, v162
	v_min_f32_e32 v168, 0x40e00000, v70
	v_exp_f32_e32 v70, v1
	v_mul_f32_e32 v1, 0xc01d265f, v163
	v_min_f32_e32 v169, 0x40e00000, v71
	v_exp_f32_e32 v71, v1
	v_mul_f32_e32 v1, 0xc01d265f, v168
	v_exp_f32_e32 v170, v1
	v_mul_f32_e32 v1, 0xc01d265f, v169
	v_exp_f32_e32 v171, v1
	v_pk_add_f32 v[70:71], v[70:71], 1.0 op_sel_hi:[1,0]
	v_pk_fma_f32 v[166:167], v[28:29], s[24:25], v[150:151] op_sel_hi:[1,0,1]
	v_rcp_f32_e32 v70, v70
	v_rcp_f32_e32 v71, v71
	v_pk_add_f32 v[170:171], v[170:171], 1.0 op_sel_hi:[1,0]
	v_med3_f32 v166, v166, s62, v159
	v_med3_f32 v167, v167, s62, v159
	v_rcp_f32_e32 v170, v170
	v_rcp_f32_e32 v171, v171
	v_pk_mul_f32 v[70:71], v[162:163], v[70:71]
	v_pk_fma_f32 v[164:165], v[30:31], s[24:25], v[148:149] op_sel_hi:[1,0,1]
	v_pk_mul_f32 v[162:163], v[166:167], v[70:71]
	v_mov_b32_e32 v70, 0
	v_mov_b32_e32 v71, 0
	v_cvt_pk_fp8_f32 v70, v156, v157
	v_cvt_pk_fp8_f32 v71, v162, v163
	v_med3_f32 v164, v164, s62, v159
	v_med3_f32 v165, v165, s62, v159
	v_pk_mul_f32 v[156:157], v[168:169], v[170:171]
	v_cvt_pk_fp8_f32 v70, v160, v161 op_sel:[0,0,1]
	v_pk_mul_f32 v[156:157], v[164:165], v[156:157]
	v_pk_fma_f32 v[160:161], v[32:33], s[24:25], v[154:155] op_sel_hi:[1,0,1]
	v_cvt_pk_fp8_f32 v71, v156, v157 op_sel:[0,0,1]
	v_add_co_u32_e32 v156, vcc, s59, v146
	v_permlane16_swap_b32_e32 v68, v70
	v_permlane16_swap_b32_e32 v69, v71
	v_addc_co_u32_e32 v157, vcc, 0, v147, vcc
	global_store_dwordx4 v[156:157], v[68:71], off
	v_med3_f32 v160, v160, s62, v159
	v_med3_f32 v161, v161, s62, v159
	v_pk_fma_f32 v[70:71], v[64:65], s[24:25], v[136:137] op_sel_hi:[1,0,1]
	v_pk_fma_f32 v[68:69], v[66:67], s[24:25], v[138:139] op_sel_hi:[1,0,1]
	v_min_f32_e32 v70, 0x40e00000, v70
	v_min_f32_e32 v71, 0x40e00000, v71
	v_mul_f32_e32 v1, 0xc01d265f, v70
	v_min_f32_e32 v68, 0x40e00000, v68
	v_exp_f32_e32 v162, v1
	v_mul_f32_e32 v1, 0xc01d265f, v71
	v_min_f32_e32 v69, 0x40e00000, v69
	v_mul_f32_e32 v141, 0xc01d265f, v68
	v_exp_f32_e32 v163, v1
	v_exp_f32_e32 v164, v141
	v_mul_f32_e32 v141, 0xc01d265f, v69
	v_exp_f32_e32 v165, v141
	v_pk_add_f32 v[162:163], v[162:163], 1.0 op_sel_hi:[1,0]
	v_pk_fma_f32 v[156:157], v[34:35], s[24:25], v[152:153] op_sel_hi:[1,0,1]
	v_rcp_f32_e32 v162, v162
	v_rcp_f32_e32 v163, v163
	v_pk_add_f32 v[164:165], v[164:165], 1.0 op_sel_hi:[1,0]
	v_med3_f32 v156, v156, s62, v159
	v_rcp_f32_e32 v164, v164
	v_rcp_f32_e32 v165, v165
	v_pk_mul_f32 v[70:71], v[70:71], v[162:163]
	v_med3_f32 v157, v157, s62, v159
	v_pk_mul_f32 v[70:71], v[160:161], v[70:71]
	v_pk_fma_f32 v[160:161], v[60:61], s[24:25], v[132:133] op_sel_hi:[1,0,1]
	v_pk_mul_f32 v[68:69], v[68:69], v[164:165]
	v_min_f32_e32 v160, 0x40e00000, v160
	v_pk_mul_f32 v[156:157], v[156:157], v[68:69]
	v_pk_fma_f32 v[68:69], v[62:63], s[24:25], v[134:135] op_sel_hi:[1,0,1]
	v_min_f32_e32 v161, 0x40e00000, v161
	v_mul_f32_e32 v1, 0xc01d265f, v160
	v_min_f32_e32 v166, 0x40e00000, v68
	v_exp_f32_e32 v68, v1
	v_mul_f32_e32 v1, 0xc01d265f, v161
	v_min_f32_e32 v167, 0x40e00000, v69
	v_exp_f32_e32 v69, v1
	v_mul_f32_e32 v1, 0xc01d265f, v166
	v_exp_f32_e32 v168, v1
	v_mul_f32_e32 v1, 0xc01d265f, v167
	v_pk_add_f32 v[68:69], v[68:69], 1.0 op_sel_hi:[1,0]
	v_exp_f32_e32 v169, v1
	v_rcp_f32_e32 v68, v68
	v_rcp_f32_e32 v69, v69
	v_pk_fma_f32 v[164:165], v[232:233], s[24:25], v[150:151] op_sel_hi:[1,0,1]
	v_pk_add_f32 v[168:169], v[168:169], 1.0 op_sel_hi:[1,0]
	v_med3_f32 v164, v164, s62, v159
	v_med3_f32 v165, v165, s62, v159
	v_pk_mul_f32 v[68:69], v[160:161], v[68:69]
	v_rcp_f32_e32 v168, v168
	v_pk_mul_f32 v[160:161], v[164:165], v[68:69]
	v_mov_b32_e32 v68, 0
	v_rcp_f32_e32 v169, v169
	v_cvt_pk_fp8_f32 v68, v70, v71
	v_mov_b32_e32 v69, 0
	v_cvt_pk_fp8_f32 v69, v160, v161
	v_pk_fma_f32 v[162:163], v[234:235], s[24:25], v[148:149] op_sel_hi:[1,0,1]
	v_pk_mul_f32 v[70:71], v[166:167], v[168:169]
	v_med3_f32 v162, v162, s62, v159
	v_med3_f32 v163, v163, s62, v159
	v_cvt_pk_fp8_f32 v68, v156, v157 op_sel:[0,0,1]
	v_pk_fma_f32 v[156:157], v[56:57], s[24:25], v[136:137] op_sel_hi:[1,0,1]
	v_pk_mul_f32 v[70:71], v[162:163], v[70:71]
	v_min_f32_e32 v156, 0x40e00000, v156
	v_cvt_pk_fp8_f32 v69, v70, v71 op_sel:[0,0,1]
	v_pk_fma_f32 v[70:71], v[58:59], s[24:25], v[138:139] op_sel_hi:[1,0,1]
	v_min_f32_e32 v157, 0x40e00000, v157
	v_mul_f32_e32 v1, 0xc01d265f, v156
	v_min_f32_e32 v70, 0x40e00000, v70
	v_exp_f32_e32 v164, v1
	v_mul_f32_e32 v1, 0xc01d265f, v157
	v_min_f32_e32 v71, 0x40e00000, v71
	v_mul_f32_e32 v141, 0xc01d265f, v70
	v_exp_f32_e32 v165, v1
	v_exp_f32_e32 v166, v141
	v_mul_f32_e32 v141, 0xc01d265f, v71
	v_exp_f32_e32 v167, v141
	v_pk_add_f32 v[164:165], v[164:165], 1.0 op_sel_hi:[1,0]
	v_pk_fma_f32 v[162:163], v[24:25], s[24:25], v[154:155] op_sel_hi:[1,0,1]
	v_rcp_f32_e32 v164, v164
	v_rcp_f32_e32 v165, v165
	v_pk_add_f32 v[166:167], v[166:167], 1.0 op_sel_hi:[1,0]
	v_med3_f32 v162, v162, s62, v159
	v_rcp_f32_e32 v166, v166
	v_rcp_f32_e32 v167, v167
	v_med3_f32 v163, v163, s62, v159
	v_pk_mul_f32 v[156:157], v[156:157], v[164:165]
	v_pk_fma_f32 v[160:161], v[26:27], s[24:25], v[152:153] op_sel_hi:[1,0,1]
	v_pk_mul_f32 v[156:157], v[162:163], v[156:157]
	v_pk_fma_f32 v[162:163], v[52:53], s[24:25], v[132:133] op_sel_hi:[1,0,1]
	v_med3_f32 v160, v160, s62, v159
	v_med3_f32 v161, v161, s62, v159
	v_pk_mul_f32 v[70:71], v[70:71], v[166:167]
	v_min_f32_e32 v162, 0x40e00000, v162
	v_pk_mul_f32 v[160:161], v[160:161], v[70:71]
	v_pk_fma_f32 v[70:71], v[54:55], s[24:25], v[134:135] op_sel_hi:[1,0,1]
	v_min_f32_e32 v163, 0x40e00000, v163
	v_mul_f32_e32 v1, 0xc01d265f, v162
	v_min_f32_e32 v168, 0x40e00000, v70
	v_exp_f32_e32 v70, v1
	v_mul_f32_e32 v1, 0xc01d265f, v163
	v_min_f32_e32 v169, 0x40e00000, v71
	v_exp_f32_e32 v71, v1
	v_mul_f32_e32 v1, 0xc01d265f, v168
	v_exp_f32_e32 v170, v1
	v_mul_f32_e32 v1, 0xc01d265f, v169
	v_exp_f32_e32 v171, v1
	v_pk_add_f32 v[70:71], v[70:71], 1.0 op_sel_hi:[1,0]
	v_pk_fma_f32 v[166:167], v[20:21], s[24:25], v[150:151] op_sel_hi:[1,0,1]
	v_rcp_f32_e32 v70, v70
	v_rcp_f32_e32 v71, v71
	v_pk_add_f32 v[170:171], v[170:171], 1.0 op_sel_hi:[1,0]
	v_med3_f32 v166, v166, s62, v159
	v_med3_f32 v167, v167, s62, v159
	v_rcp_f32_e32 v170, v170
	v_rcp_f32_e32 v171, v171
	v_pk_mul_f32 v[70:71], v[162:163], v[70:71]
	v_pk_fma_f32 v[164:165], v[22:23], s[24:25], v[148:149] op_sel_hi:[1,0,1]
	v_pk_mul_f32 v[162:163], v[166:167], v[70:71]
	v_mov_b32_e32 v70, 0
	v_mov_b32_e32 v71, 0
	v_cvt_pk_fp8_f32 v70, v156, v157
	v_cvt_pk_fp8_f32 v71, v162, v163
	v_med3_f32 v164, v164, s62, v159
	v_med3_f32 v165, v165, s62, v159
	v_pk_mul_f32 v[156:157], v[168:169], v[170:171]
	v_cvt_pk_fp8_f32 v70, v160, v161 op_sel:[0,0,1]
	v_pk_mul_f32 v[156:157], v[164:165], v[156:157]
	v_pk_fma_f32 v[160:161], v[16:17], s[24:25], v[154:155] op_sel_hi:[1,0,1]
	v_cvt_pk_fp8_f32 v71, v156, v157 op_sel:[0,0,1]
	v_add_co_u32_e32 v156, vcc, s63, v146
	v_permlane16_swap_b32_e32 v68, v70
	v_permlane16_swap_b32_e32 v69, v71
	v_addc_co_u32_e32 v157, vcc, 0, v147, vcc
	global_store_dwordx4 v[156:157], v[68:71], off
	v_med3_f32 v160, v160, s62, v159
	v_med3_f32 v161, v161, s62, v159
	v_pk_fma_f32 v[70:71], v[48:49], s[24:25], v[136:137] op_sel_hi:[1,0,1]
	v_pk_fma_f32 v[68:69], v[50:51], s[24:25], v[138:139] op_sel_hi:[1,0,1]
	v_min_f32_e32 v70, 0x40e00000, v70
	v_min_f32_e32 v71, 0x40e00000, v71
	v_mul_f32_e32 v1, 0xc01d265f, v70
	v_min_f32_e32 v68, 0x40e00000, v68
	v_exp_f32_e32 v162, v1
	v_mul_f32_e32 v1, 0xc01d265f, v71
	v_min_f32_e32 v69, 0x40e00000, v69
	v_mul_f32_e32 v141, 0xc01d265f, v68
	v_exp_f32_e32 v163, v1
	v_exp_f32_e32 v164, v141
	v_mul_f32_e32 v141, 0xc01d265f, v69
	v_exp_f32_e32 v165, v141
	v_pk_add_f32 v[162:163], v[162:163], 1.0 op_sel_hi:[1,0]
	v_pk_fma_f32 v[156:157], v[18:19], s[24:25], v[152:153] op_sel_hi:[1,0,1]
	v_rcp_f32_e32 v162, v162
	v_rcp_f32_e32 v163, v163
	v_pk_add_f32 v[164:165], v[164:165], 1.0 op_sel_hi:[1,0]
	v_med3_f32 v156, v156, s62, v159
	v_rcp_f32_e32 v164, v164
	v_rcp_f32_e32 v165, v165
	v_pk_mul_f32 v[70:71], v[70:71], v[162:163]
	v_med3_f32 v157, v157, s62, v159
	v_pk_mul_f32 v[70:71], v[160:161], v[70:71]
	v_pk_fma_f32 v[160:161], v[44:45], s[24:25], v[132:133] op_sel_hi:[1,0,1]
	v_pk_mul_f32 v[68:69], v[68:69], v[164:165]
	v_min_f32_e32 v160, 0x40e00000, v160
	v_pk_mul_f32 v[156:157], v[156:157], v[68:69]
	v_pk_fma_f32 v[68:69], v[46:47], s[24:25], v[134:135] op_sel_hi:[1,0,1]
	v_min_f32_e32 v161, 0x40e00000, v161
	v_mul_f32_e32 v1, 0xc01d265f, v160
	v_min_f32_e32 v166, 0x40e00000, v68
	v_exp_f32_e32 v68, v1
	v_mul_f32_e32 v1, 0xc01d265f, v161
	v_min_f32_e32 v167, 0x40e00000, v69
	v_exp_f32_e32 v69, v1
	v_mul_f32_e32 v1, 0xc01d265f, v166
	v_exp_f32_e32 v168, v1
	v_mul_f32_e32 v1, 0xc01d265f, v167
	v_exp_f32_e32 v169, v1
	v_pk_add_f32 v[68:69], v[68:69], 1.0 op_sel_hi:[1,0]
	v_pk_fma_f32 v[164:165], v[12:13], s[24:25], v[150:151] op_sel_hi:[1,0,1]
	v_rcp_f32_e32 v68, v68
	v_rcp_f32_e32 v69, v69
	v_pk_add_f32 v[168:169], v[168:169], 1.0 op_sel_hi:[1,0]
	v_med3_f32 v164, v164, s62, v159
	v_med3_f32 v165, v165, s62, v159
	v_rcp_f32_e32 v168, v168
	v_rcp_f32_e32 v169, v169
	v_pk_mul_f32 v[68:69], v[160:161], v[68:69]
	v_pk_fma_f32 v[162:163], v[14:15], s[24:25], v[148:149] op_sel_hi:[1,0,1]
	v_pk_mul_f32 v[160:161], v[164:165], v[68:69]
	v_mov_b32_e32 v69, 0
	v_cvt_pk_fp8_f32 v69, v160, v161
	v_mov_b32_e32 v68, 0
	v_med3_f32 v162, v162, s62, v159
	v_med3_f32 v163, v163, s62, v159
	v_cvt_pk_fp8_f32 v68, v70, v71
	v_pk_mul_f32 v[70:71], v[166:167], v[168:169]
	v_pk_fma_f32 v[136:137], v[40:41], s[24:25], v[136:137] op_sel_hi:[1,0,1]
	v_pk_mul_f32 v[70:71], v[162:163], v[70:71]
	v_cvt_pk_fp8_f32 v68, v156, v157 op_sel:[0,0,1]
	v_cvt_pk_fp8_f32 v69, v70, v71 op_sel:[0,0,1]
	v_pk_fma_f32 v[70:71], v[42:43], s[24:25], v[138:139] op_sel_hi:[1,0,1]
	v_min_f32_e32 v136, 0x40e00000, v136
	v_min_f32_e32 v70, 0x40e00000, v70
	v_min_f32_e32 v71, 0x40e00000, v71
	v_mul_f32_e32 v141, 0xc01d265f, v70
	v_exp_f32_e32 v156, v141
	v_mul_f32_e32 v141, 0xc01d265f, v71
	v_exp_f32_e32 v157, v141
	v_min_f32_e32 v137, 0x40e00000, v137
	v_mul_f32_e32 v1, 0xc01d265f, v136
	v_pk_fma_f32 v[138:139], v[10:11], s[24:25], v[152:153] op_sel_hi:[1,0,1]
	v_pk_fma_f32 v[152:153], v[8:9], s[24:25], v[154:155] op_sel_hi:[1,0,1]
	v_exp_f32_e32 v154, v1
	v_mul_f32_e32 v1, 0xc01d265f, v137
	v_pk_add_f32 v[156:157], v[156:157], 1.0 op_sel_hi:[1,0]
	v_exp_f32_e32 v155, v1
	v_rcp_f32_e32 v156, v156
	v_rcp_f32_e32 v157, v157
	v_pk_fma_f32 v[132:133], v[36:37], s[24:25], v[132:133] op_sel_hi:[1,0,1]
	v_pk_add_f32 v[154:155], v[154:155], 1.0 op_sel_hi:[1,0]
	v_med3_f32 v138, v138, s62, v159
	v_med3_f32 v139, v139, s62, v159
	v_pk_mul_f32 v[70:71], v[70:71], v[156:157]
	v_min_f32_e32 v132, 0x40e00000, v132
	v_rcp_f32_e32 v154, v154
	v_rcp_f32_e32 v155, v155
	v_pk_mul_f32 v[138:139], v[138:139], v[70:71]
	v_pk_fma_f32 v[70:71], v[38:39], s[24:25], v[134:135] op_sel_hi:[1,0,1]
	v_min_f32_e32 v133, 0x40e00000, v133
	v_mul_f32_e32 v1, 0xc01d265f, v132
	v_pk_fma_f32 v[134:135], v[6:7], s[24:25], v[148:149] op_sel_hi:[1,0,1]
	v_pk_fma_f32 v[148:149], v[4:5], s[24:25], v[150:151] op_sel_hi:[1,0,1]
	v_min_f32_e32 v150, 0x40e00000, v70
	v_exp_f32_e32 v70, v1
	v_mul_f32_e32 v1, 0xc01d265f, v133
	v_min_f32_e32 v151, 0x40e00000, v71
	v_exp_f32_e32 v71, v1
	v_med3_f32 v152, v152, s62, v159
	v_med3_f32 v153, v153, s62, v159
	v_pk_mul_f32 v[136:137], v[136:137], v[154:155]
	v_mul_f32_e32 v1, 0xc01d265f, v150
	v_pk_mul_f32 v[136:137], v[152:153], v[136:137]
	v_exp_f32_e32 v152, v1
	v_mul_f32_e32 v1, 0xc01d265f, v151
	v_exp_f32_e32 v153, v1
	v_pk_add_f32 v[70:71], v[70:71], 1.0 op_sel_hi:[1,0]
	v_med3_f32 v148, v148, s62, v159
	v_rcp_f32_e32 v70, v70
	v_rcp_f32_e32 v71, v71
	v_pk_add_f32 v[152:153], v[152:153], 1.0 op_sel_hi:[1,0]
	v_med3_f32 v149, v149, s62, v159
	v_rcp_f32_e32 v152, v152
	v_rcp_f32_e32 v153, v153
	v_pk_mul_f32 v[70:71], v[132:133], v[70:71]
	v_med3_f32 v134, v134, s62, v159
	v_pk_mul_f32 v[132:133], v[148:149], v[70:71]
	v_mov_b32_e32 v70, 0
	v_mov_b32_e32 v71, 0
	v_cvt_pk_fp8_f32 v70, v136, v137
	v_cvt_pk_fp8_f32 v71, v132, v133
	v_med3_f32 v135, v135, s62, v159
	v_pk_mul_f32 v[132:133], v[150:151], v[152:153]
	v_cvt_pk_fp8_f32 v70, v138, v139 op_sel:[0,0,1]
	v_pk_mul_f32 v[132:133], v[134:135], v[132:133]
	s_nop 0
	v_permlane16_swap_b32_e32 v68, v70
	v_cvt_pk_fp8_f32 v71, v132, v133 op_sel:[0,0,1]
	v_add_co_u32_e32 v132, vcc, 0x50000, v146
	s_nop 0
	v_permlane16_swap_b32_e32 v69, v71
	v_addc_co_u32_e32 v133, vcc, 0, v147, vcc
	s_andn2_b64 vcc, exec, s[36:37]
	global_store_dwordx4 v[132:133], v[68:71], off
	s_cbranch_vccnz .LBB0_888
	s_waitcnt vmcnt(4)
	v_xor_b32_e32 v204, 0x400, v204
	ds_write_b128 v204, v[184:187]
	ds_write_b128 v204, v[188:191] offset:16
	ds_write_b128 v204, v[192:195] offset:512
	ds_write_b128 v204, v[196:199] offset:528
	ds_read_b128 v[0:3], v253
	s_andn2_b64 vcc, exec, s[20:21]
	s_cbranch_vccnz .LBB0_887
	s_barrier
	s_branch .LBB0_887
